# row reductions in N1/N2/FIN: 6-hop ds_bpermute butterfly replaced by DPP reduction + readlane (same summation tree)
# speedup vs baseline: 1.0271x; 1.0018x over previous
.LBB0_131:
	s_waitcnt vmcnt(4)
	v_cvt_pk_f32_fp8_e32 v[24:25], v54
	v_cvt_pk_f32_fp8_sdwa v[108:109], v54 src0_sel:WORD_1
	s_waitcnt vmcnt(3)
	v_cvt_pk_f32_fp8_e32 v[110:111], v58
	v_cvt_pk_f32_fp8_sdwa v[112:113], v58 src0_sel:WORD_1
	v_lshlrev_b32_e32 v16, 16, v14
	v_and_b32_e32 v17, 0xffff0000, v14
	v_lshlrev_b32_e32 v14, 16, v15
	v_and_b32_e32 v15, 0xffff0000, v15
	v_pk_add_f32 v[24:25], v[24:25], v[110:111]
	v_pk_add_f32 v[108:109], v[108:109], v[112:113]
	s_ashr_i32 s83, s82, 31
	v_pk_fma_f32 v[106:107], v[106:107], v[108:109], v[14:15]
	v_pk_fma_f32 v[14:15], v[104:105], v[24:25], v[16:17]
	v_cvt_pk_f32_fp8_e32 v[16:17], v55
	v_cvt_pk_f32_fp8_sdwa v[24:25], v55 src0_sel:WORD_1
	v_cvt_pk_f32_fp8_e32 v[54:55], v59
	v_cvt_pk_f32_fp8_sdwa v[58:59], v59 src0_sel:WORD_1
	v_lshlrev_b32_e32 v104, 16, v18
	v_and_b32_e32 v105, 0xffff0000, v18
	v_pk_add_f32 v[16:17], v[16:17], v[54:55]
	v_pk_add_f32 v[24:25], v[24:25], v[58:59]
	v_lshlrev_b32_e32 v18, 16, v19
	v_and_b32_e32 v19, 0xffff0000, v19
	v_pk_fma_f32 v[18:19], v[102:103], v[24:25], v[18:19]
	v_pk_fma_f32 v[16:17], v[100:101], v[16:17], v[104:105]
	v_cvt_pk_f32_fp8_e32 v[24:25], v56
	v_cvt_pk_f32_fp8_sdwa v[100:101], v56 src0_sel:WORD_1
	v_cvt_pk_f32_fp8_e32 v[102:103], v60
	v_cvt_pk_f32_fp8_sdwa v[104:105], v60 src0_sel:WORD_1
	v_cvt_pk_bf16_f32 v14, v14, v15
	v_cvt_pk_bf16_f32 v15, v106, v107
	v_cvt_pk_bf16_f32 v16, v16, v17
	v_cvt_pk_bf16_f32 v17, v18, v19
	v_pk_add_f32 v[18:19], v[24:25], v[102:103]
	v_and_b32_e32 v59, 0xffff0000, v15
	v_pk_add_f32 v[24:25], v[100:101], v[104:105]
	v_lshlrev_b32_e32 v106, 16, v22
	v_and_b32_e32 v107, 0xffff0000, v22
	v_lshlrev_b32_e32 v22, 16, v23
	v_and_b32_e32 v23, 0xffff0000, v23
	v_lshlrev_b32_e32 v58, 16, v15
	v_mul_f32_e32 v56, v59, v59
	v_pk_fma_f32 v[24:25], v[98:99], v[24:25], v[22:23]
	v_pk_fma_f32 v[100:101], v[58:59], v[58:59], v[56:57] op_sel_hi:[1,1,0]
	v_pk_fma_f32 v[18:19], v[96:97], v[18:19], v[106:107]
	v_cvt_pk_f32_fp8_e32 v[96:97], v61
	v_cvt_pk_bf16_f32 v22, v18, v19
	v_cvt_pk_bf16_f32 v23, v24, v25
	v_cvt_pk_f32_fp8_e32 v[24:25], v57
	v_cvt_pk_f32_fp8_sdwa v[56:57], v57 src0_sel:WORD_1
	v_cvt_pk_f32_fp8_sdwa v[60:61], v61 src0_sel:WORD_1
	v_lshlrev_b32_e32 v18, 16, v26
	v_and_b32_e32 v19, 0xffff0000, v26
	v_lshlrev_b32_e32 v26, 16, v27
	v_and_b32_e32 v27, 0xffff0000, v27
	v_pk_add_f32 v[56:57], v[56:57], v[60:61]
	v_and_b32_e32 v55, 0xffff0000, v14
	v_pk_add_f32 v[24:25], v[24:25], v[96:97]
	v_pk_fma_f32 v[26:27], v[94:95], v[56:57], v[26:27]
	v_lshlrev_b32_e32 v54, 16, v14
	v_and_b32_e32 v105, 0xffff0000, v17
	v_and_b32_e32 v104, 0xffff0000, v16
	v_pk_fma_f32 v[18:19], v[92:93], v[24:25], v[18:19]
	v_lshlrev_b32_e32 v102, 16, v16
	v_cvt_pk_bf16_f32 v24, v18, v19
	v_cvt_pk_bf16_f32 v25, v26, v27
	v_mul_f32_e32 v26, v55, v55
	v_lshlrev_b32_e32 v27, 16, v24
	v_lshlrev_b32_e32 v103, 16, v17
	v_pk_mul_f32 v[18:19], v[104:105], v[104:105]
	v_pk_fma_f32 v[96:97], v[54:55], v[54:55], v[26:27] op_sel_hi:[1,1,0]
	v_and_b32_e32 v57, 0xffff0000, v24
	v_pk_fma_f32 v[18:19], v[102:103], v[102:103], v[18:19]
	v_mov_b32_e32 v26, v96
	v_mov_b32_e32 v98, v100
	v_mov_b32_e32 v99, v27
	v_and_b32_e32 v93, 0xffff0000, v22
	v_mul_f32_e32 v1, v57, v57
	v_pk_add_f32 v[96:97], v[96:97], v[100:101]
	v_pk_mul_f32 v[98:99], v[26:27], v[98:99]
	v_pk_add_f32 v[18:19], v[18:19], v[18:19] op_sel:[0,1] op_sel_hi:[1,0]
	v_lshlrev_b32_e32 v92, 16, v22
	v_and_b32_e32 v95, 0xffff0000, v23
	v_mov_b32_e32 v97, v99
	v_mov_b32_e32 v19, v1
	v_mul_f32_e32 v26, v93, v93
	v_lshlrev_b32_e32 v60, 16, v25
	v_and_b32_e32 v61, 0xffff0000, v25
	v_lshlrev_b32_e32 v94, 16, v23
	v_pk_add_f32 v[18:19], v[96:97], v[18:19]
	v_pk_fma_f32 v[96:97], v[92:93], v[92:93], v[26:27] op_sel_hi:[1,1,0]
	v_mul_f32_e32 v26, v95, v95
	v_mul_f32_e32 v56, v60, v60
	v_mul_f32_e32 v67, v61, v61
	v_pk_fma_f32 v[98:99], v[94:95], v[94:95], v[26:27] op_sel_hi:[1,1,0]
	v_mov_b32_e32 v97, v56
	v_mov_b32_e32 v99, v67
	v_pk_add_f32 v[96:97], v[96:97], v[98:99]
	v_mov_b32_e32 v56, v27
	v_pk_add_f32 v[18:19], v[18:19], v[96:97]
	s_lshl_b64 s[48:49], s[82:83], 10
	v_add_f32_e32 v1, v18, v19
	s_lshl_b64 s[50:51], s[82:83], 11
	s_waitcnt lgkmcnt(0)
	s_nop 1
	v_add_f32_dpp v1, v1, v1 quad_perm:[1,0,3,2] row_mask:0xf bank_mask:0xf
	s_waitcnt lgkmcnt(0)
	s_nop 1
	v_add_f32_dpp v1, v1, v1 quad_perm:[2,3,0,1] row_mask:0xf bank_mask:0xf
	s_waitcnt lgkmcnt(0)
	s_nop 1
	v_add_f32_dpp v1, v1, v1 row_half_mirror row_mask:0xf bank_mask:0xf
	s_waitcnt lgkmcnt(0)
	s_nop 1
	v_add_f32_dpp v1, v1, v1 row_mirror row_mask:0xf bank_mask:0xf
	s_waitcnt lgkmcnt(0)
	s_nop 1
	v_add_f32_dpp v1, v1, v1 row_bcast:15 row_mask:0xa bank_mask:0xf
	s_waitcnt lgkmcnt(0)
	s_nop 1
	v_add_f32_dpp v1, v1, v1 row_bcast:31 row_mask:0xc bank_mask:0xf
	s_nop 0
	v_readlane_b32 s101, v1, 63
	s_nop 1
	v_mov_b32_e32 v1, s101
	v_fmamk_f32 v1, v1, 0x3a800000, v210
	v_rsq_f32_e32 v26, v1
	s_nop 0
	v_pk_mul_f32 v[18:19], v[26:27], v[54:55] op_sel_hi:[0,1]
	v_pk_fma_f32 v[28:29], v[18:19], v[28:29], v[62:63]
	v_mov_b32_e32 v18, v0
	v_cvt_pk_fp8_f32 v18, v28, v29
	v_pk_mul_f32 v[54:55], v[26:27], v[58:59] op_sel_hi:[0,1]
	v_pk_fma_f32 v[20:21], v[54:55], v[20:21], v[64:65]
	v_mov_b32_e32 v19, v0
	v_cvt_pk_fp8_f32 v18, v20, v21 op_sel:[0,0,1]
	v_mov_b32_e32 v20, v102
	v_mov_b32_e32 v21, v104
	v_pk_mul_f32 v[20:21], v[26:27], v[20:21] op_sel_hi:[0,1]
	v_pk_fma_f32 v[10:11], v[20:21], v[90:91], v[10:11]
	v_mov_b32_e32 v104, v103
	v_cvt_pk_fp8_f32 v19, v10, v11
	v_pk_mul_f32 v[10:11], v[26:27], v[104:105] op_sel_hi:[0,1]
	v_pk_fma_f32 v[10:11], v[10:11], v[88:89], v[12:13]
	v_mov_b32_e32 v20, v0
	v_cvt_pk_fp8_f32 v19, v10, v11 op_sel:[0,0,1]
	v_pk_mul_f32 v[10:11], v[26:27], v[92:93] op_sel_hi:[0,1]
	v_pk_fma_f32 v[6:7], v[10:11], v[86:87], v[6:7]
	v_mov_b32_e32 v21, v0
	v_cvt_pk_fp8_f32 v20, v6, v7
	v_pk_mul_f32 v[6:7], v[26:27], v[56:57] op_sel_hi:[0,1]
	v_pk_fma_f32 v[2:3], v[6:7], v[82:83], v[2:3]
	v_pk_mul_f32 v[12:13], v[26:27], v[94:95] op_sel_hi:[0,1]
	v_cvt_pk_fp8_f32 v21, v2, v3
	v_pk_mul_f32 v[2:3], v[26:27], v[60:61] op_sel_hi:[0,1]
	v_pk_fma_f32 v[8:9], v[12:13], v[84:85], v[8:9]
	v_pk_fma_f32 v[2:3], v[2:3], v[80:81], v[4:5]
	v_cvt_pk_fp8_f32 v20, v8, v9 op_sel:[0,0,1]
	v_cvt_pk_fp8_f32 v21, v2, v3 op_sel:[0,0,1]
	v_lshl_add_u64 v[28:29], v[76:77], 0, s[50:51]
	v_lshl_add_u64 v[2:3], v[70:71], 0, s[48:49]
	global_store_dwordx4 v[28:29], v[14:17], off
	global_store_dwordx4 v[28:29], v[22:25], off offset:16
	global_store_dwordx4 v[2:3], v[18:21], off
	v_mov_b64_e32 v[14:15], v[30:31]
	v_mov_b64_e32 v[22:23], v[38:39]
	v_mov_b64_e32 v[18:19], v[34:35]
	v_mov_b64_e32 v[26:27], v[42:43]
	s_waitcnt vmcnt(4)
	v_mov_b32_e32 v54, v50
	v_mov_b32_e32 v55, v51
	v_mov_b32_e32 v56, v52
	v_mov_b32_e32 v57, v53
	s_waitcnt vmcnt(3)
	v_mov_b32_e32 v58, v46
	v_mov_b32_e32 v59, v47
	v_mov_b32_e32 v60, v48
	v_mov_b32_e32 v61, v49
	v_mov_b64_e32 v[16:17], v[32:33]
	v_mov_b64_e32 v[20:21], v[36:37]
	v_mov_b64_e32 v[24:25], v[40:41]
	v_mov_b64_e32 v[28:29], v[44:45]
	s_cmp_lt_i32 s86, s26
	s_mov_b32 s82, s86
	s_cbranch_scc0 .LBB0_142

.LBB0_134:
	s_waitcnt vmcnt(6)
	v_lshlrev_b32_e32 v16, 16, v30
	v_and_b32_e32 v17, 0xffff0000, v30
	v_lshlrev_b32_e32 v24, 16, v31
	v_and_b32_e32 v25, 0xffff0000, v31
	s_waitcnt vmcnt(4)
	v_cvt_pk_f32_fp8_e32 v[30:31], v50
	v_cvt_pk_f32_fp8_sdwa v[34:35], v50 src0_sel:WORD_1
	s_waitcnt vmcnt(3)
	v_cvt_pk_f32_fp8_e32 v[42:43], v46
	v_cvt_pk_f32_fp8_sdwa v[124:125], v46 src0_sel:WORD_1
	s_add_i32 s84, s84, 4
	s_add_i32 s86, s82, 1
	v_pk_add_f32 v[30:31], v[30:31], v[42:43]
	v_pk_add_f32 v[34:35], v[34:35], v[124:125]
	v_pk_fma_f32 v[16:17], v[104:105], v[30:31], v[16:17]
	v_pk_fma_f32 v[24:25], v[106:107], v[34:35], v[24:25]
	v_cvt_pk_bf16_f32 v124, v16, v17
	v_cvt_pk_f32_fp8_e32 v[16:17], v51
	v_cvt_pk_bf16_f32 v125, v24, v25
	v_cvt_pk_f32_fp8_sdwa v[24:25], v51 src0_sel:WORD_1
	v_cvt_pk_f32_fp8_e32 v[30:31], v47
	v_cvt_pk_f32_fp8_sdwa v[34:35], v47 src0_sel:WORD_1
	v_lshlrev_b32_e32 v42, 16, v38
	v_and_b32_e32 v43, 0xffff0000, v38
	v_pk_add_f32 v[16:17], v[16:17], v[30:31]
	v_pk_add_f32 v[24:25], v[24:25], v[34:35]
	v_lshlrev_b32_e32 v34, 16, v32
	v_and_b32_e32 v35, 0xffff0000, v32
	v_lshlrev_b32_e32 v32, 16, v33
	v_and_b32_e32 v33, 0xffff0000, v33
	v_pk_fma_f32 v[24:25], v[102:103], v[24:25], v[32:33]
	v_pk_fma_f32 v[16:17], v[100:101], v[16:17], v[34:35]
	v_cvt_pk_f32_fp8_e32 v[32:33], v48
	v_cvt_pk_bf16_f32 v126, v16, v17
	v_cvt_pk_bf16_f32 v127, v24, v25
	v_cvt_pk_f32_fp8_e32 v[16:17], v52
	v_cvt_pk_f32_fp8_sdwa v[24:25], v52 src0_sel:WORD_1
	v_cvt_pk_f32_fp8_sdwa v[34:35], v48 src0_sel:WORD_1
	v_lshlrev_b32_e32 v38, 16, v39
	v_pk_add_f32 v[32:33], v[16:17], v[32:33]
	v_and_b32_e32 v39, 0xffff0000, v39
	v_pk_add_f32 v[24:25], v[24:25], v[34:35]
	v_pk_fma_f32 v[32:33], v[96:97], v[32:33], v[42:43]
	v_pk_fma_f32 v[24:25], v[98:99], v[24:25], v[38:39]
	v_cvt_pk_bf16_f32 v128, v32, v33
	v_cvt_pk_f32_fp8_sdwa v[32:33], v53 src0_sel:WORD_1
	v_cvt_pk_bf16_f32 v129, v24, v25
	v_cvt_pk_f32_fp8_e32 v[24:25], v53
	v_cvt_pk_f32_fp8_e32 v[38:39], v49
	v_cvt_pk_f32_fp8_sdwa v[42:43], v49 src0_sel:WORD_1
	v_and_b32_e32 v31, 0xffff0000, v124
	v_and_b32_e32 v133, 0xffff0000, v125
	v_pk_add_f32 v[24:25], v[24:25], v[38:39]
	v_pk_add_f32 v[32:33], v[32:33], v[42:43]
	v_lshlrev_b32_e32 v42, 16, v40
	v_and_b32_e32 v43, 0xffff0000, v40
	v_pk_fma_f32 v[24:25], v[92:93], v[24:25], v[42:43]
	v_lshlrev_b32_e32 v30, 16, v124
	v_lshlrev_b32_e32 v132, 16, v125
	v_mul_f32_e32 v16, v133, v133
	v_lshlrev_b32_e32 v40, 16, v41
	v_and_b32_e32 v41, 0xffff0000, v41
	v_cvt_pk_bf16_f32 v130, v24, v25
	v_mul_f32_e32 v24, v31, v31
	v_lshlrev_b32_e32 v25, 16, v130
	v_pk_fma_f32 v[134:135], v[132:133], v[132:133], v[16:17] op_sel_hi:[1,1,0]
	v_and_b32_e32 v17, 0xffff0000, v127
	v_and_b32_e32 v16, 0xffff0000, v126
	v_pk_fma_f32 v[32:33], v[94:95], v[32:33], v[40:41]
	v_pk_fma_f32 v[40:41], v[30:31], v[30:31], v[24:25] op_sel_hi:[1,1,0]
	v_lshlrev_b32_e32 v34, 16, v126
	v_lshlrev_b32_e32 v35, 16, v127
	v_pk_mul_f32 v[38:39], v[16:17], v[16:17]
	v_cvt_pk_bf16_f32 v131, v32, v33
	global_store_dwordx4 v[112:113], v[124:127], off
	global_store_dwordx4 v[114:115], v[128:131], off offset:16
	v_mov_b32_e32 v24, v40
	v_mov_b32_e32 v112, v134
	v_mov_b32_e32 v113, v25
	v_pk_fma_f32 v[136:137], v[34:35], v[34:35], v[38:39]
	v_and_b32_e32 v43, 0xffff0000, v130
	v_pk_add_f32 v[40:41], v[40:41], v[134:135]
	v_pk_mul_f32 v[112:113], v[24:25], v[112:113]
	v_and_b32_e32 v39, 0xffff0000, v128
	v_mul_f32_e32 v1, v43, v43
	v_mov_b32_e32 v41, v113
	v_pk_add_f32 v[112:113], v[136:137], v[136:137] op_sel:[0,1] op_sel_hi:[1,0]
	v_lshlrev_b32_e32 v38, 16, v128
	v_and_b32_e32 v139, 0xffff0000, v129
	v_mov_b32_e32 v113, v1
	v_mul_f32_e32 v24, v39, v39
	v_lshlrev_b32_e32 v138, 16, v129
	v_lshlrev_b32_e32 v32, 16, v131
	v_and_b32_e32 v33, 0xffff0000, v131
	v_pk_add_f32 v[40:41], v[40:41], v[112:113]
	v_pk_fma_f32 v[112:113], v[38:39], v[38:39], v[24:25] op_sel_hi:[1,1,0]
	v_mul_f32_e32 v24, v139, v139
	v_mul_f32_e32 v42, v32, v32
	v_mul_f32_e32 v67, v33, v33
	v_pk_fma_f32 v[114:115], v[138:139], v[138:139], v[24:25] op_sel_hi:[1,1,0]
	v_mov_b32_e32 v113, v42
	v_mov_b32_e32 v115, v67
	v_pk_add_f32 v[112:113], v[112:113], v[114:115]
	v_mov_b32_e32 v42, v25
	v_pk_add_f32 v[40:41], v[40:41], v[112:113]
	v_lshl_add_u64 v[44:45], v[44:45], 0, s[28:29]
	v_add_f32_e32 v1, v40, v41
	v_lshl_add_u64 v[108:109], v[108:109], 0, s[34:35]
	v_lshl_add_u64 v[110:111], v[110:111], 0, s[28:29]
	s_cmp_lt_i32 s86, s17
	s_waitcnt lgkmcnt(0)
	s_nop 1
	v_add_f32_dpp v1, v1, v1 quad_perm:[1,0,3,2] row_mask:0xf bank_mask:0xf
	s_waitcnt lgkmcnt(0)
	s_nop 1
	v_add_f32_dpp v1, v1, v1 quad_perm:[2,3,0,1] row_mask:0xf bank_mask:0xf
	s_waitcnt lgkmcnt(0)
	s_nop 1
	v_add_f32_dpp v1, v1, v1 row_half_mirror row_mask:0xf bank_mask:0xf
	s_waitcnt lgkmcnt(0)
	s_nop 1
	v_add_f32_dpp v1, v1, v1 row_mirror row_mask:0xf bank_mask:0xf
	s_waitcnt lgkmcnt(0)
	s_nop 1
	v_add_f32_dpp v1, v1, v1 row_bcast:15 row_mask:0xa bank_mask:0xf
	s_waitcnt lgkmcnt(0)
	s_nop 1
	v_add_f32_dpp v1, v1, v1 row_bcast:31 row_mask:0xc bank_mask:0xf
	s_nop 0
	v_readlane_b32 s101, v1, 63
	s_nop 1
	v_mov_b32_e32 v1, s101
	v_fmamk_f32 v1, v1, 0x3a800000, v210
	v_rsq_f32_e32 v24, v1
	s_nop 0
	v_pk_mul_f32 v[40:41], v[24:25], v[30:31] op_sel_hi:[0,1]
	v_pk_mul_f32 v[112:113], v[24:25], v[132:133] op_sel_hi:[0,1]
	v_pk_fma_f32 v[114:115], v[112:113], v[20:21], v[64:65]
	v_pk_fma_f32 v[40:41], v[40:41], v[28:29], v[62:63]
	v_mov_b32_e32 v112, v0
	v_cvt_pk_fp8_f32 v112, v40, v41
	v_mov_b32_e32 v40, v34
	v_mov_b32_e32 v41, v16
	v_pk_mul_f32 v[40:41], v[24:25], v[40:41] op_sel_hi:[0,1]
	v_pk_fma_f32 v[40:41], v[40:41], v[90:91], v[10:11]
	v_mov_b32_e32 v113, v0
	v_cvt_pk_fp8_f32 v113, v40, v41
	v_cvt_pk_fp8_f32 v112, v114, v115 op_sel:[0,0,1]
	v_mov_b32_e32 v114, v35
	v_mov_b32_e32 v115, v17
	v_pk_mul_f32 v[114:115], v[24:25], v[114:115] op_sel_hi:[0,1]
	v_pk_fma_f32 v[114:115], v[114:115], v[88:89], v[12:13]
	v_pk_mul_f32 v[40:41], v[24:25], v[38:39] op_sel_hi:[0,1]
	v_cvt_pk_fp8_f32 v113, v114, v115 op_sel:[0,0,1]
	v_pk_mul_f32 v[114:115], v[24:25], v[138:139] op_sel_hi:[0,1]
	v_pk_fma_f32 v[124:125], v[114:115], v[84:85], v[8:9]
	v_pk_fma_f32 v[40:41], v[40:41], v[86:87], v[6:7]
	v_mov_b32_e32 v114, v0
	v_cvt_pk_fp8_f32 v114, v40, v41
	v_pk_mul_f32 v[40:41], v[24:25], v[42:43] op_sel_hi:[0,1]
	v_pk_fma_f32 v[40:41], v[40:41], v[82:83], v[2:3]
	v_mov_b32_e32 v115, v0
	v_cvt_pk_fp8_f32 v115, v40, v41
	v_pk_mul_f32 v[32:33], v[24:25], v[32:33] op_sel_hi:[0,1]
	v_pk_fma_f32 v[32:33], v[32:33], v[80:81], v[4:5]
	v_cvt_pk_fp8_f32 v114, v124, v125 op_sel:[0,0,1]
	v_cvt_pk_fp8_f32 v115, v32, v33 op_sel:[0,0,1]
	v_lshl_add_u64 v[32:33], s[80:81], 0, v[36:37]
	v_lshl_add_u64 v[36:37], v[36:37], 0, s[34:35]
	global_store_dwordx4 v[32:33], v[112:115], off
	s_cbranch_scc0 .LBB0_137
.LBB0_135:
	s_waitcnt vmcnt(4)
	v_cvt_pk_f32_fp8_e32 v[24:25], v54
	v_cvt_pk_f32_fp8_sdwa v[34:35], v54 src0_sel:WORD_1
	s_waitcnt vmcnt(3)
	v_cvt_pk_f32_fp8_e32 v[42:43], v58
	v_cvt_pk_f32_fp8_sdwa v[124:125], v58 src0_sel:WORD_1
	v_lshl_add_u64 v[16:17], s[80:81], 0, v[44:45]
	s_mov_b64 s[48:49], 0x18200000
	s_ashr_i32 s85, s84, 31
	v_lshl_add_u64 v[112:113], v[16:17], 0, s[48:49]
	v_add_co_u32_e32 v114, vcc, s79, v16
	s_lshl_b64 s[48:49], s[84:85], 10
	s_nop 0
	v_addc_co_u32_e32 v115, vcc, 0, v17, vcc
	v_lshl_add_u64 v[16:17], v[78:79], 0, s[48:49]
	global_load_dwordx4 v[30:33], v[114:115], off
	global_load_dwordx4 v[38:41], v[112:113], off offset:16
	global_load_dwordx4 v[50:53], v[16:17], off
	global_load_dwordx4 v[46:49], v[16:17], off offset:1024
	v_lshlrev_b32_e32 v16, 16, v14
	v_and_b32_e32 v17, 0xffff0000, v14
	v_lshlrev_b32_e32 v14, 16, v15
	v_and_b32_e32 v15, 0xffff0000, v15
	v_pk_add_f32 v[24:25], v[24:25], v[42:43]
	v_pk_add_f32 v[34:35], v[34:35], v[124:125]
	v_pk_fma_f32 v[16:17], v[104:105], v[24:25], v[16:17]
	v_pk_fma_f32 v[14:15], v[106:107], v[34:35], v[14:15]
	v_cvt_pk_f32_fp8_e32 v[24:25], v55
	v_cvt_pk_f32_fp8_sdwa v[34:35], v55 src0_sel:WORD_1
	v_cvt_pk_f32_fp8_e32 v[42:43], v59
	v_cvt_pk_f32_fp8_sdwa v[126:127], v59 src0_sel:WORD_1
	v_cvt_pk_bf16_f32 v124, v16, v17
	v_cvt_pk_f32_fp8_e32 v[128:129], v60
	v_pk_add_f32 v[16:17], v[24:25], v[42:43]
	v_pk_add_f32 v[24:25], v[34:35], v[126:127]
	v_lshlrev_b32_e32 v42, 16, v18
	v_and_b32_e32 v43, 0xffff0000, v18
	v_lshlrev_b32_e32 v18, 16, v19
	v_and_b32_e32 v19, 0xffff0000, v19
	v_pk_fma_f32 v[18:19], v[102:103], v[24:25], v[18:19]
	v_pk_fma_f32 v[16:17], v[100:101], v[16:17], v[42:43]
	v_cvt_pk_f32_fp8_e32 v[24:25], v56
	v_cvt_pk_f32_fp8_sdwa v[42:43], v56 src0_sel:WORD_1
	v_cvt_pk_f32_fp8_sdwa v[130:131], v60 src0_sel:WORD_1
	v_cvt_pk_bf16_f32 v125, v14, v15
	v_cvt_pk_bf16_f32 v126, v16, v17
	v_cvt_pk_bf16_f32 v127, v18, v19
	v_pk_add_f32 v[16:17], v[24:25], v[128:129]
	v_pk_add_f32 v[18:19], v[42:43], v[130:131]
	v_lshlrev_b32_e32 v128, 16, v22
	v_and_b32_e32 v129, 0xffff0000, v22
	v_lshlrev_b32_e32 v22, 16, v23
	v_and_b32_e32 v23, 0xffff0000, v23
	v_cvt_pk_f32_fp8_sdwa v[130:131], v57 src0_sel:WORD_1
	v_cvt_pk_f32_fp8_sdwa v[136:137], v61 src0_sel:WORD_1
	v_pk_fma_f32 v[18:19], v[98:99], v[18:19], v[22:23]
	v_cvt_pk_f32_fp8_e32 v[22:23], v57
	v_cvt_pk_f32_fp8_e32 v[134:135], v61
	v_pk_fma_f32 v[16:17], v[96:97], v[16:17], v[128:129]
	v_and_b32_e32 v15, 0xffff0000, v124
	v_cvt_pk_bf16_f32 v128, v16, v17
	v_cvt_pk_bf16_f32 v129, v18, v19
	v_pk_add_f32 v[18:19], v[130:131], v[136:137]
	v_lshlrev_b32_e32 v130, 16, v26
	v_and_b32_e32 v131, 0xffff0000, v26
	v_lshlrev_b32_e32 v26, 16, v27
	v_and_b32_e32 v27, 0xffff0000, v27
	v_and_b32_e32 v35, 0xffff0000, v125
	v_pk_add_f32 v[16:17], v[22:23], v[134:135]
	v_pk_fma_f32 v[18:19], v[94:95], v[18:19], v[26:27]
	v_lshlrev_b32_e32 v14, 16, v124
	v_lshlrev_b32_e32 v34, 16, v125
	v_mul_f32_e32 v24, v35, v35
	v_pk_fma_f32 v[16:17], v[92:93], v[16:17], v[130:131]
	v_pk_fma_f32 v[24:25], v[34:35], v[34:35], v[24:25] op_sel_hi:[1,1,0]
	v_cvt_pk_bf16_f32 v130, v16, v17
	v_cvt_pk_bf16_f32 v131, v18, v19
	v_mul_f32_e32 v18, v15, v15
	v_and_b32_e32 v133, 0xffff0000, v127
	v_and_b32_e32 v132, 0xffff0000, v126
	v_lshlrev_b32_e32 v26, 16, v130
	v_pk_fma_f32 v[18:19], v[14:15], v[14:15], v[18:19] op_sel_hi:[1,1,0]
	v_lshlrev_b32_e32 v42, 16, v126
	v_lshlrev_b32_e32 v43, 16, v127
	v_pk_mul_f32 v[22:23], v[132:133], v[132:133]
	v_mov_b32_e32 v138, v18
	v_mov_b32_e32 v139, v26
	v_mov_b32_e32 v140, v24
	v_mov_b32_e32 v141, v26
	v_pk_fma_f32 v[134:135], v[42:43], v[42:43], v[22:23]
	v_and_b32_e32 v27, 0xffff0000, v130
	v_pk_add_f32 v[18:19], v[18:19], v[24:25]
	v_pk_mul_f32 v[24:25], v[138:139], v[140:141]
	v_mul_f32_e32 v1, v27, v27
	v_mov_b32_e32 v19, v25
	v_pk_add_f32 v[24:25], v[134:135], v[134:135] op_sel:[0,1] op_sel_hi:[1,0]
	v_and_b32_e32 v23, 0xffff0000, v128
	v_and_b32_e32 v137, 0xffff0000, v129
	v_mov_b32_e32 v25, v1
	v_lshlrev_b32_e32 v22, 16, v128
	v_lshlrev_b32_e32 v136, 16, v129
	v_lshlrev_b32_e32 v16, 16, v131
	v_and_b32_e32 v17, 0xffff0000, v131
	v_pk_add_f32 v[18:19], v[18:19], v[24:25]
	v_mul_f32_e32 v24, v23, v23
	v_mul_f32_e32 v134, v137, v137
	v_mul_f32_e32 v67, v16, v16
	v_mul_f32_e32 v75, v17, v17
	v_pk_fma_f32 v[24:25], v[22:23], v[22:23], v[24:25] op_sel_hi:[1,1,0]
	v_pk_fma_f32 v[134:135], v[136:137], v[136:137], v[134:135] op_sel_hi:[1,1,0]
	v_mov_b32_e32 v25, v67
	v_mov_b32_e32 v135, v75
	v_pk_add_f32 v[24:25], v[24:25], v[134:135]
	s_add_i32 s82, s82, 2
	v_pk_add_f32 v[18:19], v[18:19], v[24:25]
	v_lshl_add_u64 v[24:25], s[80:81], 0, v[110:111]
	v_add_f32_e32 v1, v18, v19
	v_add_co_u32_e32 v24, vcc, s79, v24
	v_mov_b32_e32 v19, v132
	s_nop 0
	v_addc_co_u32_e32 v25, vcc, 0, v25, vcc
	s_waitcnt lgkmcnt(0)
	s_nop 1
	v_add_f32_dpp v1, v1, v1 quad_perm:[1,0,3,2] row_mask:0xf bank_mask:0xf
	global_store_dwordx4 v[24:25], v[124:127], off
	global_store_dwordx4 v[24:25], v[128:131], off offset:16
	s_cmp_ge_i32 s82, s26
	s_waitcnt lgkmcnt(0)
	s_nop 1
	v_add_f32_dpp v1, v1, v1 quad_perm:[2,3,0,1] row_mask:0xf bank_mask:0xf
	s_waitcnt lgkmcnt(0)
	s_nop 1
	v_add_f32_dpp v1, v1, v1 row_half_mirror row_mask:0xf bank_mask:0xf
	s_waitcnt lgkmcnt(0)
	s_nop 1
	v_add_f32_dpp v1, v1, v1 row_mirror row_mask:0xf bank_mask:0xf
	s_waitcnt lgkmcnt(0)
	s_nop 1
	v_add_f32_dpp v1, v1, v1 row_bcast:15 row_mask:0xa bank_mask:0xf
	v_mov_b32_e32 v18, v42
	s_waitcnt lgkmcnt(0)
	s_nop 1
	v_add_f32_dpp v1, v1, v1 row_bcast:31 row_mask:0xc bank_mask:0xf
	s_nop 0
	v_readlane_b32 s101, v1, 63
	s_nop 1
	v_mov_b32_e32 v1, s101
	v_fmamk_f32 v1, v1, 0x3a800000, v210
	v_rsq_f32_e32 v134, v1
	s_nop 0
	v_pk_mul_f32 v[124:125], v[134:135], v[14:15] op_sel_hi:[0,1]
	v_pk_fma_f32 v[126:127], v[124:125], v[28:29], v[62:63]
	v_mov_b32_e32 v124, v0
	v_cvt_pk_fp8_f32 v124, v126, v127
	v_pk_mul_f32 v[24:25], v[134:135], v[34:35] op_sel_hi:[0,1]
	v_pk_fma_f32 v[24:25], v[24:25], v[20:21], v[64:65]
	v_mov_b32_e32 v125, v0
	v_cvt_pk_fp8_f32 v124, v24, v25 op_sel:[0,0,1]
	v_mov_b32_e32 v24, v42
	v_mov_b32_e32 v25, v132
	v_pk_mul_f32 v[24:25], v[134:135], v[24:25] op_sel_hi:[0,1]
	v_pk_fma_f32 v[24:25], v[24:25], v[90:91], v[10:11]
	v_mov_b32_e32 v132, v43
	v_cvt_pk_fp8_f32 v125, v24, v25
	v_pk_mul_f32 v[24:25], v[134:135], v[132:133] op_sel_hi:[0,1]
	v_pk_fma_f32 v[24:25], v[24:25], v[88:89], v[12:13]
	v_mov_b32_e32 v126, v0
	v_cvt_pk_fp8_f32 v125, v24, v25 op_sel:[0,0,1]
	v_pk_mul_f32 v[24:25], v[134:135], v[22:23] op_sel_hi:[0,1]
	v_pk_fma_f32 v[24:25], v[24:25], v[86:87], v[6:7]
	v_mov_b32_e32 v127, v0
	v_cvt_pk_fp8_f32 v126, v24, v25
	v_pk_mul_f32 v[24:25], v[134:135], v[26:27] op_sel_hi:[0,1]
	v_pk_fma_f32 v[24:25], v[24:25], v[82:83], v[2:3]
	v_pk_mul_f32 v[34:35], v[134:135], v[136:137] op_sel_hi:[0,1]
	v_cvt_pk_fp8_f32 v127, v24, v25
	v_pk_mul_f32 v[16:17], v[134:135], v[16:17] op_sel_hi:[0,1]
	v_pk_fma_f32 v[34:35], v[34:35], v[84:85], v[8:9]
	v_pk_fma_f32 v[16:17], v[16:17], v[80:81], v[4:5]
	v_cvt_pk_fp8_f32 v126, v34, v35 op_sel:[0,0,1]
	v_cvt_pk_fp8_f32 v127, v16, v17 op_sel:[0,0,1]
	v_lshl_add_u64 v[16:17], s[80:81], 0, v[108:109]
	global_store_dwordx4 v[16:17], v[124:127], off
	s_cbranch_scc1 .LBB0_134
	s_ashr_i32 s83, s82, 31
	s_lshl_b64 s[48:49], s[82:83], 11
	v_lshl_add_u64 v[14:15], v[76:77], 0, s[48:49]
	s_add_i32 s48, s84, 2
	s_ashr_i32 s49, s48, 31
	s_lshl_b64 s[48:49], s[48:49], 10
	global_load_dwordx4 v[22:25], v[14:15], off offset:16
	s_nop 0
	global_load_dwordx4 v[14:17], v[14:15], off
	v_lshl_add_u64 v[18:19], v[78:79], 0, s[48:49]
	global_load_dwordx4 v[54:57], v[18:19], off
	global_load_dwordx4 v[58:61], v[18:19], off offset:1024
	s_waitcnt vmcnt(3)
	v_mov_b32_e32 v26, v24
	s_waitcnt vmcnt(2)
	v_mov_b32_e32 v18, v16
	v_mov_b32_e32 v19, v17
	v_mov_b32_e32 v27, v25
	s_branch .LBB0_134

.LBB0_151:
	s_waitcnt vmcnt(1)
	v_pk_mul_f32 v[72:73], v[34:35], v[34:35]
	v_pk_mul_f32 v[74:75], v[32:33], v[32:33]
	v_mul_f32_e32 v1, v4, v4
	v_pk_mov_b32 v[76:77], v[74:75], v[72:73] op_sel:[1,0]
	v_mov_b32_e32 v75, v73
	v_pk_add_f32 v[72:73], v[76:77], v[74:75]
	v_pk_mul_f32 v[74:75], v[30:31], v[30:31]
	v_pk_mul_f32 v[76:77], v[28:29], v[28:29]
	v_mul_f32_e32 v53, v5, v5
	v_pk_mov_b32 v[84:85], v[76:77], v[74:75] op_sel:[1,0]
	v_mov_b32_e32 v77, v75
	v_pk_add_f32 v[74:75], v[84:85], v[76:77]
	v_pk_add_f32 v[72:73], v[72:73], v[72:73] op_sel:[0,1] op_sel_hi:[1,0]
	v_pk_add_f32 v[74:75], v[74:75], v[74:75] op_sel:[0,1] op_sel_hi:[1,0]
	v_mov_b32_e32 v73, v1
	v_mov_b32_e32 v75, v53
	v_pk_add_f32 v[72:73], v[72:73], v[74:75]
	v_mul_f32_e32 v74, v9, v9
	v_mul_f32_e32 v76, v6, v6
	v_pk_fma_f32 v[74:75], v[8:9], v[8:9], v[74:75] op_sel_hi:[1,1,0]
	v_mul_f32_e32 v84, v7, v7
	v_mov_b32_e32 v75, v76
	v_mul_f32_e32 v76, v11, v11
	v_pk_fma_f32 v[76:77], v[10:11], v[10:11], v[76:77] op_sel_hi:[1,1,0]
	s_ashr_i32 s1, s0, 31
	v_mov_b32_e32 v77, v84
	v_pk_add_f32 v[74:75], v[74:75], v[76:77]
	s_lshl_b64 s[0:1], s[0:1], 10
	v_pk_add_f32 v[72:73], v[72:73], v[74:75]
	s_mov_b32 s16, s22
	v_add_f32_e32 v1, v72, v73
	s_waitcnt lgkmcnt(0)
	s_nop 1
	v_add_f32_dpp v1, v1, v1 quad_perm:[1,0,3,2] row_mask:0xf bank_mask:0xf
	s_waitcnt lgkmcnt(0)
	s_nop 1
	v_add_f32_dpp v1, v1, v1 quad_perm:[2,3,0,1] row_mask:0xf bank_mask:0xf
	s_waitcnt lgkmcnt(0)
	s_nop 1
	v_add_f32_dpp v1, v1, v1 row_half_mirror row_mask:0xf bank_mask:0xf
	s_waitcnt lgkmcnt(0)
	s_nop 1
	v_add_f32_dpp v1, v1, v1 row_mirror row_mask:0xf bank_mask:0xf
	s_waitcnt lgkmcnt(0)
	s_nop 1
	v_add_f32_dpp v1, v1, v1 row_bcast:15 row_mask:0xa bank_mask:0xf
	s_waitcnt lgkmcnt(0)
	s_nop 1
	v_add_f32_dpp v1, v1, v1 row_bcast:31 row_mask:0xc bank_mask:0xf
	s_nop 0
	v_readlane_b32 s101, v1, 63
	s_nop 1
	v_mov_b32_e32 v1, s101
	v_fmamk_f32 v1, v1, 0x3a800000, v210
	v_rsq_f32_e32 v72, v1
	s_nop 0
	v_pk_mul_f32 v[32:33], v[72:73], v[32:33] op_sel_hi:[0,1]
	s_waitcnt vmcnt(0)
	v_pk_fma_f32 v[48:49], v[32:33], v[66:67], v[48:49]
	v_mov_b32_e32 v32, v0
	v_cvt_pk_fp8_f32 v32, v48, v49
	v_pk_mul_f32 v[34:35], v[72:73], v[34:35] op_sel_hi:[0,1]
	v_pk_fma_f32 v[34:35], v[34:35], v[64:65], v[50:51]
	v_pk_mul_f32 v[28:29], v[72:73], v[28:29] op_sel_hi:[0,1]
	v_pk_mul_f32 v[8:9], v[72:73], v[8:9] op_sel_hi:[0,1]
	v_pk_mul_f32 v[4:5], v[72:73], v[4:5] op_sel_hi:[0,1]
	v_cvt_pk_fp8_f32 v32, v34, v35 op_sel:[0,0,1]
	v_pk_fma_f32 v[28:29], v[28:29], v[70:71], v[44:45]
	v_mov_b32_e32 v33, v0
	v_pk_fma_f32 v[8:9], v[8:9], v[62:63], v[40:41]
	v_mov_b32_e32 v34, v0
	v_pk_fma_f32 v[2:3], v[4:5], v[2:3], v[36:37]
	v_mov_b32_e32 v35, v0
	v_cvt_pk_fp8_f32 v33, v28, v29
	v_cvt_pk_fp8_f32 v34, v8, v9
	v_cvt_pk_fp8_f32 v35, v2, v3
	v_pk_mul_f32 v[30:31], v[72:73], v[30:31] op_sel_hi:[0,1]
	v_pk_mul_f32 v[10:11], v[72:73], v[10:11] op_sel_hi:[0,1]
	v_pk_mul_f32 v[6:7], v[72:73], v[6:7] op_sel_hi:[0,1]
	v_pk_fma_f32 v[30:31], v[30:31], v[68:69], v[46:47]
	v_pk_fma_f32 v[10:11], v[10:11], v[60:61], v[42:43]
	v_pk_fma_f32 v[6:7], v[6:7], v[58:59], v[38:39]
	v_cvt_pk_fp8_f32 v33, v30, v31 op_sel:[0,0,1]
	v_cvt_pk_fp8_f32 v34, v10, v11 op_sel:[0,0,1]
	v_cvt_pk_fp8_f32 v35, v6, v7 op_sel:[0,0,1]
	v_lshl_add_u64 v[2:3], v[54:55], 0, s[0:1]
	v_mov_b64_e32 v[4:5], v[12:13]
	v_mov_b64_e32 v[8:9], v[16:17]
	global_store_dwordx4 v[2:3], v[32:35], off
	v_mov_b64_e32 v[30:31], v[22:23]
	v_mov_b64_e32 v[6:7], v[14:15]
	v_mov_b64_e32 v[34:35], v[26:27]
	v_mov_b64_e32 v[10:11], v[18:19]
	v_mov_b64_e32 v[28:29], v[20:21]
	v_mov_b64_e32 v[32:33], v[24:25]
	s_cmp_ge_i32 s16, s26
	s_cbranch_scc1 .LBB0_127

.LBB0_158:
	s_ashr_i32 s23, s22, 31
	s_lshl_b64 s[10:11], s[22:23], 12
	s_add_u32 s0, s0, s10
	s_addc_u32 s1, s1, s11
	global_load_dwordx4 v[12:15], v72, s[0:1] offset:48
	global_load_dwordx4 v[16:19], v72, s[0:1] offset:32
	global_load_dwordx4 v[20:23], v72, s[0:1] offset:16
	global_load_dwordx4 v[24:27], v72, s[0:1]
	s_waitcnt vmcnt(5)
	v_pk_mul_f32 v[84:85], v[34:35], v[34:35]
	v_pk_mul_f32 v[86:87], v[32:33], v[32:33]
	v_mul_f32_e32 v1, v4, v4
	v_pk_mov_b32 v[88:89], v[86:87], v[84:85] op_sel:[1,0]
	v_mov_b32_e32 v87, v85
	v_pk_add_f32 v[84:85], v[88:89], v[86:87]
	v_pk_mul_f32 v[86:87], v[30:31], v[30:31]
	v_pk_mul_f32 v[88:89], v[28:29], v[28:29]
	v_mul_f32_e32 v53, v5, v5
	v_pk_mov_b32 v[90:91], v[88:89], v[86:87] op_sel:[1,0]
	v_mov_b32_e32 v89, v87
	v_pk_add_f32 v[86:87], v[90:91], v[88:89]
	v_pk_add_f32 v[84:85], v[84:85], v[84:85] op_sel:[0,1] op_sel_hi:[1,0]
	v_pk_add_f32 v[86:87], v[86:87], v[86:87] op_sel:[0,1] op_sel_hi:[1,0]
	v_mov_b32_e32 v85, v1
	v_mov_b32_e32 v87, v53
	v_pk_add_f32 v[84:85], v[84:85], v[86:87]
	v_mul_f32_e32 v86, v9, v9
	v_mul_f32_e32 v88, v11, v11
	v_mul_f32_e32 v73, v6, v6
	v_mul_f32_e32 v90, v7, v7
	v_pk_fma_f32 v[86:87], v[8:9], v[8:9], v[86:87] op_sel_hi:[1,1,0]
	v_pk_fma_f32 v[88:89], v[10:11], v[10:11], v[88:89] op_sel_hi:[1,1,0]
	v_mov_b32_e32 v87, v73
	v_mov_b32_e32 v89, v90
	v_pk_add_f32 v[86:87], v[86:87], v[88:89]
	s_add_i32 s1, s16, 2
	v_pk_add_f32 v[84:85], v[84:85], v[86:87]
	s_add_i32 s0, s33, 0x101
	v_add_f32_e32 v1, v84, v85
	s_cmp_ge_i32 s0, s26
	s_waitcnt lgkmcnt(0)
	s_nop 1
	v_add_f32_dpp v1, v1, v1 quad_perm:[1,0,3,2] row_mask:0xf bank_mask:0xf
	s_waitcnt lgkmcnt(0)
	s_nop 1
	v_add_f32_dpp v1, v1, v1 quad_perm:[2,3,0,1] row_mask:0xf bank_mask:0xf
	s_waitcnt lgkmcnt(0)
	s_nop 1
	v_add_f32_dpp v1, v1, v1 row_half_mirror row_mask:0xf bank_mask:0xf
	s_waitcnt lgkmcnt(0)
	s_nop 1
	v_add_f32_dpp v1, v1, v1 row_mirror row_mask:0xf bank_mask:0xf
	s_waitcnt lgkmcnt(0)
	s_nop 1
	v_add_f32_dpp v1, v1, v1 row_bcast:15 row_mask:0xa bank_mask:0xf
	s_waitcnt lgkmcnt(0)
	s_nop 1
	v_add_f32_dpp v1, v1, v1 row_bcast:31 row_mask:0xc bank_mask:0xf
	s_nop 0
	v_readlane_b32 s101, v1, 63
	s_nop 1
	v_mov_b32_e32 v1, s101
	v_fmamk_f32 v1, v1, 0x3a800000, v210
	v_rsq_f32_e32 v88, v1
	s_nop 0
	v_pk_mul_f32 v[84:85], v[88:89], v[32:33] op_sel_hi:[0,1]
	s_waitcnt vmcnt(4)
	v_pk_fma_f32 v[90:91], v[84:85], v[66:67], v[48:49]
	v_mov_b32_e32 v84, v0
	v_cvt_pk_fp8_f32 v84, v90, v91
	v_pk_mul_f32 v[90:91], v[88:89], v[28:29] op_sel_hi:[0,1]
	v_pk_fma_f32 v[90:91], v[90:91], v[70:71], v[44:45]
	v_mov_b32_e32 v85, v0
	v_pk_mul_f32 v[86:87], v[88:89], v[34:35] op_sel_hi:[0,1]
	v_cvt_pk_fp8_f32 v85, v90, v91
	v_pk_fma_f32 v[86:87], v[86:87], v[64:65], v[50:51]
	v_pk_mul_f32 v[90:91], v[88:89], v[10:11] op_sel_hi:[0,1]
	v_cvt_pk_fp8_f32 v84, v86, v87 op_sel:[0,0,1]
	v_pk_mul_f32 v[86:87], v[88:89], v[30:31] op_sel_hi:[0,1]
	v_pk_fma_f32 v[86:87], v[86:87], v[68:69], v[46:47]
	v_pk_fma_f32 v[90:91], v[90:91], v[60:61], v[42:43]
	v_cvt_pk_fp8_f32 v85, v86, v87 op_sel:[0,0,1]
	v_pk_mul_f32 v[86:87], v[88:89], v[8:9] op_sel_hi:[0,1]
	v_pk_fma_f32 v[92:93], v[86:87], v[62:63], v[40:41]
	v_mov_b32_e32 v86, v0
	v_cvt_pk_fp8_f32 v86, v92, v93
	v_pk_mul_f32 v[92:93], v[88:89], v[4:5] op_sel_hi:[0,1]
	v_pk_fma_f32 v[92:93], v[92:93], v[2:3], v[36:37]
	v_mov_b32_e32 v87, v0
	v_cvt_pk_fp8_f32 v87, v92, v93
	v_pk_mul_f32 v[88:89], v[88:89], v[6:7] op_sel_hi:[0,1]
	v_pk_fma_f32 v[88:89], v[88:89], v[58:59], v[38:39]
	v_cvt_pk_fp8_f32 v86, v90, v91 op_sel:[0,0,1]
	v_cvt_pk_fp8_f32 v87, v88, v89 op_sel:[0,0,1]
	global_store_dwordx4 v[76:77], v[84:87], off
	s_cbranch_scc1 .LBB0_164
	s_mul_hi_i32 s10, s0, 0x78787879
	s_lshr_b32 s11, s10, 31
	s_ashr_i32 s17, s10, 11
	s_add_i32 s17, s17, s11
	s_mul_i32 s23, s17, 0xffffef00
	s_add_i32 s10, s33, s23
	s_addk_i32 s10, 0x101
	s_cmpk_gt_i32 s10, 0xff
	s_cbranch_scc0 .LBB0_161
	s_lshl_b32 s10, s17, 8
	s_sub_i32 s10, s33, s10
	s_add_i32 s22, s10, 1
	s_mov_b64 s[20:21], s[12:13]
	s_cbranch_execz .LBB0_162
	s_branch .LBB0_163

.LBB0_164:
	s_waitcnt vmcnt(1)
	v_pk_mul_f32 v[84:85], v[26:27], v[26:27]
	v_pk_mul_f32 v[86:87], v[24:25], v[24:25]
	v_mul_f32_e32 v1, v12, v12
	v_pk_mov_b32 v[88:89], v[86:87], v[84:85] op_sel:[1,0]
	v_mov_b32_e32 v87, v85
	v_pk_add_f32 v[84:85], v[88:89], v[86:87]
	v_pk_mul_f32 v[86:87], v[22:23], v[22:23]
	v_pk_mul_f32 v[88:89], v[20:21], v[20:21]
	v_mul_f32_e32 v53, v13, v13
	v_pk_mov_b32 v[90:91], v[88:89], v[86:87] op_sel:[1,0]
	v_mov_b32_e32 v89, v87
	v_pk_add_f32 v[86:87], v[90:91], v[88:89]
	v_pk_add_f32 v[84:85], v[84:85], v[84:85] op_sel:[0,1] op_sel_hi:[1,0]
	v_pk_add_f32 v[86:87], v[86:87], v[86:87] op_sel:[0,1] op_sel_hi:[1,0]
	v_mov_b32_e32 v85, v1
	v_mov_b32_e32 v87, v53
	v_pk_add_f32 v[84:85], v[84:85], v[86:87]
	v_mul_f32_e32 v86, v17, v17
	v_mul_f32_e32 v88, v19, v19
	v_mul_f32_e32 v73, v14, v14
	v_mul_f32_e32 v90, v15, v15
	v_pk_fma_f32 v[86:87], v[16:17], v[16:17], v[86:87] op_sel_hi:[1,1,0]
	v_pk_fma_f32 v[88:89], v[18:19], v[18:19], v[88:89] op_sel_hi:[1,1,0]
	v_mov_b32_e32 v87, v73
	v_mov_b32_e32 v89, v90
	v_pk_add_f32 v[86:87], v[86:87], v[88:89]
	s_add_i32 s20, s16, 3
	v_pk_add_f32 v[84:85], v[84:85], v[86:87]
	s_add_i32 s10, s33, 2
	v_add_f32_e32 v1, v84, v85
	s_add_i32 s22, s33, 0x102
	v_lshl_add_u64 v[76:77], v[76:77], 0, s[34:35]
	s_cmp_lt_i32 s22, s27
	s_waitcnt lgkmcnt(0)
	s_nop 1
	v_add_f32_dpp v1, v1, v1 quad_perm:[1,0,3,2] row_mask:0xf bank_mask:0xf
	s_waitcnt lgkmcnt(0)
	s_nop 1
	v_add_f32_dpp v1, v1, v1 quad_perm:[2,3,0,1] row_mask:0xf bank_mask:0xf
	s_waitcnt lgkmcnt(0)
	s_nop 1
	v_add_f32_dpp v1, v1, v1 row_half_mirror row_mask:0xf bank_mask:0xf
	s_waitcnt lgkmcnt(0)
	s_nop 1
	v_add_f32_dpp v1, v1, v1 row_mirror row_mask:0xf bank_mask:0xf
	s_waitcnt lgkmcnt(0)
	s_nop 1
	v_add_f32_dpp v1, v1, v1 row_bcast:15 row_mask:0xa bank_mask:0xf
	s_waitcnt lgkmcnt(0)
	s_nop 1
	v_add_f32_dpp v1, v1, v1 row_bcast:31 row_mask:0xc bank_mask:0xf
	s_nop 0
	v_readlane_b32 s101, v1, 63
	s_nop 1
	v_mov_b32_e32 v1, s101
	v_fmamk_f32 v1, v1, 0x3a800000, v210
	v_rsq_f32_e32 v88, v1
	s_nop 0
	v_pk_mul_f32 v[84:85], v[88:89], v[24:25] op_sel_hi:[0,1]
	v_pk_fma_f32 v[90:91], v[84:85], v[66:67], v[48:49]
	v_mov_b32_e32 v84, v0
	v_cvt_pk_fp8_f32 v84, v90, v91
	v_pk_mul_f32 v[86:87], v[88:89], v[26:27] op_sel_hi:[0,1]
	v_pk_fma_f32 v[86:87], v[86:87], v[64:65], v[50:51]
	v_mov_b32_e32 v85, v0
	v_cvt_pk_fp8_f32 v84, v86, v87 op_sel:[0,0,1]
	v_pk_mul_f32 v[86:87], v[88:89], v[20:21] op_sel_hi:[0,1]
	v_pk_fma_f32 v[86:87], v[86:87], v[70:71], v[44:45]
	v_pk_mul_f32 v[90:91], v[88:89], v[22:23] op_sel_hi:[0,1]
	v_cvt_pk_fp8_f32 v85, v86, v87
	v_pk_mul_f32 v[86:87], v[88:89], v[16:17] op_sel_hi:[0,1]
	v_pk_fma_f32 v[92:93], v[86:87], v[62:63], v[40:41]
	v_mov_b32_e32 v86, v0
	v_cvt_pk_fp8_f32 v86, v92, v93
	v_pk_fma_f32 v[90:91], v[90:91], v[68:69], v[46:47]
	v_mov_b32_e32 v87, v0
	v_cvt_pk_fp8_f32 v85, v90, v91 op_sel:[0,0,1]
	v_pk_mul_f32 v[90:91], v[88:89], v[18:19] op_sel_hi:[0,1]
	v_pk_fma_f32 v[90:91], v[90:91], v[60:61], v[42:43]
	s_nop 0
	v_cvt_pk_fp8_f32 v86, v90, v91 op_sel:[0,0,1]
	v_pk_mul_f32 v[90:91], v[88:89], v[12:13] op_sel_hi:[0,1]
	v_pk_fma_f32 v[90:91], v[90:91], v[2:3], v[36:37]
	v_pk_mul_f32 v[88:89], v[88:89], v[14:15] op_sel_hi:[0,1]
	v_cvt_pk_fp8_f32 v87, v90, v91
	v_pk_fma_f32 v[88:89], v[88:89], v[58:59], v[38:39]
	s_nop 0
	v_cvt_pk_fp8_f32 v87, v88, v89 op_sel:[0,0,1]
	global_store_dwordx4 v[74:75], v[84:87], off
	v_lshl_add_u64 v[74:75], v[74:75], 0, s[34:35]
	s_cbranch_scc0 .LBB0_167
	s_mov_b32 s33, s10
	s_mov_b32 s16, s1
	s_branch .LBB0_154

.LBB0_783:
	s_sub_i32 s11, s10, 24
	s_min_i32 s6, s11, s2
	s_ashr_i32 s7, s6, 31
	s_lshl_b64 s[6:7], s[6:7], 11
	s_waitcnt lgkmcnt(0)
	v_lshl_add_u64 v[60:61], v[34:35], 0, s[6:7]
	global_load_dwordx2 v[66:67], v[60:61], off
	global_load_dwordx2 v[64:65], v[60:61], off offset:512
	global_load_dwordx2 v[62:63], v[60:61], off offset:1024
	s_nop 0
	global_load_dwordx2 v[60:61], v[60:61], off offset:1536
	s_waitcnt vmcnt(4)
	v_and_b32_e32 v77, 0xffff0000, v58
	v_and_b32_e32 v75, 0xffff0000, v59
	v_lshlrev_b32_e32 v76, 16, v58
	v_lshlrev_b32_e32 v74, 16, v59
	v_lshlrev_b32_e32 v72, 16, v56
	v_and_b32_e32 v73, 0xffff0000, v56
	v_lshlrev_b32_e32 v70, 16, v57
	v_and_b32_e32 v71, 0xffff0000, v57
	v_lshlrev_b32_e32 v68, 16, v54
	v_and_b32_e32 v69, 0xffff0000, v54
	v_lshlrev_b32_e32 v58, 16, v55
	v_and_b32_e32 v59, 0xffff0000, v55
	v_lshlrev_b32_e32 v56, 16, v52
	v_and_b32_e32 v57, 0xffff0000, v52
	v_lshlrev_b32_e32 v54, 16, v53
	v_and_b32_e32 v55, 0xffff0000, v53
	v_mul_f32_e32 v52, v77, v77
	v_mul_f32_e32 v53, v75, v75
	v_fmac_f32_e32 v52, v76, v76
	v_fmac_f32_e32 v53, v74, v74
	v_add_f32_e32 v52, v52, v53
	v_mul_f32_e32 v53, v73, v73
	v_mul_f32_e32 v80, v71, v71
	v_fmac_f32_e32 v53, v72, v72
	v_fmac_f32_e32 v80, v70, v70
	v_add_f32_e32 v53, v53, v80
	v_add_f32_e32 v52, v52, v53
	v_mul_f32_e32 v53, v69, v69
	v_mul_f32_e32 v80, v59, v59
	v_fmac_f32_e32 v53, v68, v68
	v_fmac_f32_e32 v80, v58, v58
	v_add_f32_e32 v53, v53, v80
	v_add_f32_e32 v52, v52, v53
	v_mul_f32_e32 v53, v57, v57
	v_mul_f32_e32 v80, v55, v55
	v_fmac_f32_e32 v53, v56, v56
	v_fmac_f32_e32 v80, v54, v54
	v_add_f32_e32 v53, v53, v80
	v_add_f32_e32 v52, v52, v53
	s_sub_i32 s13, s10, 48
	s_cmp_ge_i32 s13, s67
	s_waitcnt lgkmcnt(0)
	s_nop 1
	v_add_f32_dpp v52, v52, v52 quad_perm:[1,0,3,2] row_mask:0xf bank_mask:0xf
	s_waitcnt lgkmcnt(0)
	s_nop 1
	v_add_f32_dpp v52, v52, v52 quad_perm:[2,3,0,1] row_mask:0xf bank_mask:0xf
	s_waitcnt lgkmcnt(0)
	s_nop 1
	v_add_f32_dpp v52, v52, v52 row_half_mirror row_mask:0xf bank_mask:0xf
	s_waitcnt lgkmcnt(0)
	s_nop 1
	v_add_f32_dpp v52, v52, v52 row_mirror row_mask:0xf bank_mask:0xf
	s_waitcnt lgkmcnt(0)
	s_nop 1
	v_add_f32_dpp v52, v52, v52 row_bcast:15 row_mask:0xa bank_mask:0xf
	s_cbranch_scc1 .LBB0_789
	s_waitcnt lgkmcnt(0)
	s_nop 1
	v_add_f32_dpp v52, v52, v52 row_bcast:31 row_mask:0xc bank_mask:0xf
	s_nop 0
	v_readlane_b32 s101, v52, 63
	s_nop 1
	v_mov_b32_e32 v52, s101
	v_fmamk_f32 v52, v52, 0x3a800000, v210
	v_rsq_f32_e32 v52, v52
	s_add_i32 s6, s88, s10
	s_sub_i32 s6, s6, 48
	s_ashr_i32 s7, s6, 31
	v_pk_mul_f32 v[76:77], v[52:53], v[76:77] op_sel_hi:[0,1]
	v_pk_mul_f32 v[74:75], v[52:53], v[74:75] op_sel_hi:[0,1]
	v_pk_fma_f32 v[76:77], v[76:77], v[20:21], v[2:3]
	v_mov_b32_e32 v53, v0
	v_cvt_pk_fp8_f32 v53, v76, v77
	v_pk_fma_f32 v[74:75], v[74:75], v[18:19], v[4:5]
	v_mov_b32_e32 v76, v0
	s_lshl_b64 s[6:7], s[6:7], 10
	v_pk_mul_f32 v[72:73], v[52:53], v[72:73] op_sel_hi:[0,1]
	v_cvt_pk_fp8_f32 v53, v74, v75 op_sel:[0,0,1]
	v_pk_fma_f32 v[72:73], v[72:73], v[24:25], v[6:7]
	v_lshl_add_u64 v[80:81], v[112:113], 0, s[6:7]
	v_cvt_pk_fp8_f32 v76, v72, v73
	v_pk_mul_f32 v[70:71], v[52:53], v[70:71] op_sel_hi:[0,1]
	v_pk_fma_f32 v[70:71], v[70:71], v[22:23], v[8:9]
	v_pk_mul_f32 v[68:69], v[52:53], v[68:69] op_sel_hi:[0,1]
	v_cvt_pk_fp8_f32 v76, v70, v71 op_sel:[0,0,1]
	v_pk_fma_f32 v[68:69], v[68:69], v[28:29], v[10:11]
	v_mov_b32_e32 v70, v0
	v_pk_mul_f32 v[56:57], v[52:53], v[56:57] op_sel_hi:[0,1]
	v_cvt_pk_fp8_f32 v70, v68, v69
	v_pk_fma_f32 v[56:57], v[56:57], v[32:33], v[14:15]
	v_mov_b32_e32 v68, v0
	v_cvt_pk_fp8_f32 v68, v56, v57
	v_pk_mul_f32 v[58:59], v[52:53], v[58:59] op_sel_hi:[0,1]
	v_pk_fma_f32 v[58:59], v[58:59], v[26:27], v[12:13]
	v_pk_mul_f32 v[54:55], v[52:53], v[54:55] op_sel_hi:[0,1]
	v_cvt_pk_fp8_f32 v70, v58, v59 op_sel:[0,0,1]
	v_pk_fma_f32 v[54:55], v[54:55], v[30:31], v[16:17]
	s_nop 0
	v_cvt_pk_fp8_f32 v68, v54, v55 op_sel:[0,0,1]
	global_store_dword v[80:81], v53, off
	global_store_dword v[80:81], v76, off offset:256
	global_store_dword v[80:81], v70, off offset:512
	global_store_dword v[80:81], v68, off offset:768
	s_and_saveexec_b64 s[6:7], s[4:5]
	s_cbranch_execz .LBB0_788
	s_sub_i32 s14, s9, 32
	s_and_b32 s14, s14, 0x3ffffff0
	v_lshl_add_u32 v53, s14, 2, v161
	ds_read_b32 v54, v53
	s_cmpk_lt_i32 s13, 0x80
	s_cbranch_scc1 .LBB0_787
	s_waitcnt lgkmcnt(0)
	ds_read2st64_b32 v[54:55], v79 offset1:4
	s_waitcnt lgkmcnt(0)
	v_add_f32_e32 v54, 0, v54
	v_add_f32_e32 v56, v54, v55
	ds_read2st64_b32 v[54:55], v79 offset0:8 offset1:12
	s_waitcnt lgkmcnt(0)
	v_add_f32_e32 v54, v56, v54
	v_add_f32_e32 v56, v54, v55
	ds_read2st64_b32 v[54:55], v79 offset0:16 offset1:20
	s_waitcnt lgkmcnt(0)
	v_add_f32_e32 v54, v56, v54
	v_add_f32_e32 v56, v54, v55
	ds_read2st64_b32 v[54:55], v79 offset0:24 offset1:28
	s_waitcnt lgkmcnt(0)
	v_add_f32_e32 v54, v56, v54
	v_add_f32_e32 v54, v54, v55

.LBB0_789:
	s_add_i32 s6, s10, -16
	s_min_i32 s6, s6, s2
	s_ashr_i32 s7, s6, 31
	s_lshl_b64 s[6:7], s[6:7], 11
	s_waitcnt lgkmcnt(0)
	v_lshl_add_u64 v[52:53], v[34:35], 0, s[6:7]
	global_load_dwordx2 v[58:59], v[52:53], off
	global_load_dwordx2 v[56:57], v[52:53], off offset:512
	global_load_dwordx2 v[54:55], v[52:53], off offset:1024
	s_nop 0
	global_load_dwordx2 v[52:53], v[52:53], off offset:1536
	v_and_b32_e32 v77, 0xffff0000, v50
	v_and_b32_e32 v75, 0xffff0000, v51
	v_lshlrev_b32_e32 v76, 16, v50
	v_lshlrev_b32_e32 v74, 16, v51
	v_lshlrev_b32_e32 v72, 16, v48
	v_and_b32_e32 v73, 0xffff0000, v48
	v_lshlrev_b32_e32 v70, 16, v49
	v_and_b32_e32 v71, 0xffff0000, v49
	v_lshlrev_b32_e32 v68, 16, v46
	v_and_b32_e32 v69, 0xffff0000, v46
	v_lshlrev_b32_e32 v50, 16, v47
	v_and_b32_e32 v51, 0xffff0000, v47
	v_lshlrev_b32_e32 v48, 16, v44
	v_and_b32_e32 v49, 0xffff0000, v44
	v_lshlrev_b32_e32 v46, 16, v45
	v_and_b32_e32 v47, 0xffff0000, v45
	v_mul_f32_e32 v44, v77, v77
	v_mul_f32_e32 v45, v75, v75
	v_fmac_f32_e32 v44, v76, v76
	v_fmac_f32_e32 v45, v74, v74
	v_add_f32_e32 v44, v44, v45
	v_mul_f32_e32 v45, v73, v73
	v_mul_f32_e32 v80, v71, v71
	v_fmac_f32_e32 v45, v72, v72
	v_fmac_f32_e32 v80, v70, v70
	v_add_f32_e32 v45, v45, v80
	v_add_f32_e32 v44, v44, v45
	v_mul_f32_e32 v45, v69, v69
	v_mul_f32_e32 v80, v51, v51
	v_fmac_f32_e32 v45, v68, v68
	v_fmac_f32_e32 v80, v50, v50
	v_add_f32_e32 v45, v45, v80
	v_add_f32_e32 v44, v44, v45
	v_mul_f32_e32 v45, v49, v49
	v_mul_f32_e32 v80, v47, v47
	v_fmac_f32_e32 v45, v48, v48
	v_fmac_f32_e32 v80, v46, v46
	v_add_f32_e32 v45, v45, v80
	v_add_f32_e32 v44, v44, v45
	s_sub_i32 s13, s10, 40
	s_cmp_ge_i32 s13, s67
	s_waitcnt lgkmcnt(0)
	s_nop 1
	v_add_f32_dpp v44, v44, v44 quad_perm:[1,0,3,2] row_mask:0xf bank_mask:0xf
	s_waitcnt lgkmcnt(0)
	s_nop 1
	v_add_f32_dpp v44, v44, v44 quad_perm:[2,3,0,1] row_mask:0xf bank_mask:0xf
	s_waitcnt lgkmcnt(0)
	s_nop 1
	v_add_f32_dpp v44, v44, v44 row_half_mirror row_mask:0xf bank_mask:0xf
	s_waitcnt lgkmcnt(0)
	s_nop 1
	v_add_f32_dpp v44, v44, v44 row_mirror row_mask:0xf bank_mask:0xf
	s_waitcnt lgkmcnt(0)
	s_nop 1
	v_add_f32_dpp v44, v44, v44 row_bcast:15 row_mask:0xa bank_mask:0xf
	s_cbranch_scc1 .LBB0_795
	s_waitcnt lgkmcnt(0)
	s_nop 1
	v_add_f32_dpp v44, v44, v44 row_bcast:31 row_mask:0xc bank_mask:0xf
	s_nop 0
	v_readlane_b32 s101, v44, 63
	s_nop 1
	v_mov_b32_e32 v44, s101
	v_fmamk_f32 v44, v44, 0x3a800000, v210
	v_rsq_f32_e32 v44, v44
	s_add_i32 s6, s88, s10
	s_sub_i32 s6, s6, 40
	s_ashr_i32 s7, s6, 31
	v_pk_mul_f32 v[76:77], v[44:45], v[76:77] op_sel_hi:[0,1]
	v_pk_mul_f32 v[74:75], v[44:45], v[74:75] op_sel_hi:[0,1]
	v_pk_fma_f32 v[76:77], v[76:77], v[20:21], v[2:3]
	v_mov_b32_e32 v45, v0
	v_cvt_pk_fp8_f32 v45, v76, v77
	v_pk_fma_f32 v[74:75], v[74:75], v[18:19], v[4:5]
	v_mov_b32_e32 v76, v0
	s_lshl_b64 s[6:7], s[6:7], 10
	v_pk_mul_f32 v[72:73], v[44:45], v[72:73] op_sel_hi:[0,1]
	v_cvt_pk_fp8_f32 v45, v74, v75 op_sel:[0,0,1]
	v_pk_fma_f32 v[72:73], v[72:73], v[24:25], v[6:7]
	v_lshl_add_u64 v[80:81], v[112:113], 0, s[6:7]
	v_cvt_pk_fp8_f32 v76, v72, v73
	v_pk_mul_f32 v[70:71], v[44:45], v[70:71] op_sel_hi:[0,1]
	v_pk_fma_f32 v[70:71], v[70:71], v[22:23], v[8:9]
	v_pk_mul_f32 v[68:69], v[44:45], v[68:69] op_sel_hi:[0,1]
	v_cvt_pk_fp8_f32 v76, v70, v71 op_sel:[0,0,1]
	v_pk_fma_f32 v[68:69], v[68:69], v[28:29], v[10:11]
	v_mov_b32_e32 v70, v0
	v_pk_mul_f32 v[48:49], v[44:45], v[48:49] op_sel_hi:[0,1]
	v_cvt_pk_fp8_f32 v70, v68, v69
	v_pk_fma_f32 v[48:49], v[48:49], v[32:33], v[14:15]
	v_mov_b32_e32 v68, v0
	v_cvt_pk_fp8_f32 v68, v48, v49
	v_pk_mul_f32 v[50:51], v[44:45], v[50:51] op_sel_hi:[0,1]
	v_pk_fma_f32 v[50:51], v[50:51], v[26:27], v[12:13]
	v_pk_mul_f32 v[46:47], v[44:45], v[46:47] op_sel_hi:[0,1]
	v_cvt_pk_fp8_f32 v70, v50, v51 op_sel:[0,0,1]
	v_pk_fma_f32 v[46:47], v[46:47], v[30:31], v[16:17]
	s_nop 0
	v_cvt_pk_fp8_f32 v68, v46, v47 op_sel:[0,0,1]
	global_store_dword v[80:81], v45, off
	global_store_dword v[80:81], v76, off offset:256
	global_store_dword v[80:81], v70, off offset:512
	global_store_dword v[80:81], v68, off offset:768
	s_and_saveexec_b64 s[6:7], s[4:5]
	s_cbranch_execz .LBB0_794
	s_add_i32 s14, s9, -16
	s_and_b32 s14, s14, 0x3ffffff0
	v_lshl_add_u32 v45, s14, 2, v161
	ds_read_b32 v46, v45
	s_cmpk_lt_i32 s13, 0x80
	s_cbranch_scc1 .LBB0_793
	s_waitcnt lgkmcnt(0)
	ds_read2st64_b32 v[46:47], v79 offset0:2 offset1:6
	s_waitcnt lgkmcnt(0)
	v_add_f32_e32 v46, 0, v46
	v_add_f32_e32 v48, v46, v47
	ds_read2st64_b32 v[46:47], v79 offset0:10 offset1:14
	s_waitcnt lgkmcnt(0)
	v_add_f32_e32 v46, v48, v46
	v_add_f32_e32 v48, v46, v47
	ds_read2st64_b32 v[46:47], v79 offset0:18 offset1:22
	s_waitcnt lgkmcnt(0)
	v_add_f32_e32 v46, v48, v46
	v_add_f32_e32 v48, v46, v47
	ds_read2st64_b32 v[46:47], v79 offset0:26 offset1:30
	s_waitcnt lgkmcnt(0)
	v_add_f32_e32 v46, v48, v46
	v_add_f32_e32 v46, v46, v47

.LBB0_795:
	s_add_i32 s6, s10, -8
	s_min_i32 s6, s6, s2
	s_ashr_i32 s7, s6, 31
	s_lshl_b64 s[6:7], s[6:7], 11
	s_waitcnt lgkmcnt(0)
	v_lshl_add_u64 v[44:45], v[34:35], 0, s[6:7]
	global_load_dwordx2 v[50:51], v[44:45], off
	global_load_dwordx2 v[48:49], v[44:45], off offset:512
	global_load_dwordx2 v[46:47], v[44:45], off offset:1024
	s_nop 0
	global_load_dwordx2 v[44:45], v[44:45], off offset:1536
	v_and_b32_e32 v77, 0xffff0000, v42
	v_and_b32_e32 v75, 0xffff0000, v43
	v_lshlrev_b32_e32 v76, 16, v42
	v_lshlrev_b32_e32 v74, 16, v43
	v_lshlrev_b32_e32 v72, 16, v40
	v_and_b32_e32 v73, 0xffff0000, v40
	v_lshlrev_b32_e32 v70, 16, v41
	v_and_b32_e32 v71, 0xffff0000, v41
	v_lshlrev_b32_e32 v68, 16, v38
	v_and_b32_e32 v69, 0xffff0000, v38
	v_lshlrev_b32_e32 v42, 16, v39
	v_and_b32_e32 v43, 0xffff0000, v39
	v_lshlrev_b32_e32 v40, 16, v36
	v_and_b32_e32 v41, 0xffff0000, v36
	v_lshlrev_b32_e32 v38, 16, v37
	v_and_b32_e32 v39, 0xffff0000, v37
	v_mul_f32_e32 v36, v77, v77
	v_mul_f32_e32 v37, v75, v75
	v_fmac_f32_e32 v36, v76, v76
	v_fmac_f32_e32 v37, v74, v74
	v_add_f32_e32 v36, v36, v37
	v_mul_f32_e32 v37, v73, v73
	v_mul_f32_e32 v80, v71, v71
	v_fmac_f32_e32 v37, v72, v72
	v_fmac_f32_e32 v80, v70, v70
	v_add_f32_e32 v37, v37, v80
	v_add_f32_e32 v36, v36, v37
	v_mul_f32_e32 v37, v69, v69
	v_mul_f32_e32 v80, v43, v43
	v_fmac_f32_e32 v37, v68, v68
	v_fmac_f32_e32 v80, v42, v42
	v_add_f32_e32 v37, v37, v80
	v_add_f32_e32 v36, v36, v37
	v_mul_f32_e32 v37, v41, v41
	v_mul_f32_e32 v80, v39, v39
	v_fmac_f32_e32 v37, v40, v40
	v_fmac_f32_e32 v80, v38, v38
	v_add_f32_e32 v37, v37, v80
	v_add_f32_e32 v36, v36, v37
	s_sub_i32 s13, s10, 32
	s_cmp_ge_i32 s13, s67
	s_waitcnt lgkmcnt(0)
	s_nop 1
	v_add_f32_dpp v36, v36, v36 quad_perm:[1,0,3,2] row_mask:0xf bank_mask:0xf
	s_waitcnt lgkmcnt(0)
	s_nop 1
	v_add_f32_dpp v36, v36, v36 quad_perm:[2,3,0,1] row_mask:0xf bank_mask:0xf
	s_waitcnt lgkmcnt(0)
	s_nop 1
	v_add_f32_dpp v36, v36, v36 row_half_mirror row_mask:0xf bank_mask:0xf
	s_waitcnt lgkmcnt(0)
	s_nop 1
	v_add_f32_dpp v36, v36, v36 row_mirror row_mask:0xf bank_mask:0xf
	s_waitcnt lgkmcnt(0)
	s_nop 1
	v_add_f32_dpp v36, v36, v36 row_bcast:15 row_mask:0xa bank_mask:0xf
	s_cbranch_scc1 .LBB0_801
	s_waitcnt lgkmcnt(0)
	s_nop 1
	v_add_f32_dpp v36, v36, v36 row_bcast:31 row_mask:0xc bank_mask:0xf
	s_nop 0
	v_readlane_b32 s101, v36, 63
	s_nop 1
	v_mov_b32_e32 v36, s101
	v_fmamk_f32 v36, v36, 0x3a800000, v210
	v_rsq_f32_e32 v36, v36
	s_add_i32 s6, s88, s10
	s_sub_i32 s6, s6, 32
	s_ashr_i32 s7, s6, 31
	v_pk_mul_f32 v[76:77], v[36:37], v[76:77] op_sel_hi:[0,1]
	v_pk_mul_f32 v[74:75], v[36:37], v[74:75] op_sel_hi:[0,1]
	v_pk_fma_f32 v[76:77], v[76:77], v[20:21], v[2:3]
	v_mov_b32_e32 v37, v0
	v_cvt_pk_fp8_f32 v37, v76, v77
	v_pk_fma_f32 v[74:75], v[74:75], v[18:19], v[4:5]
	v_mov_b32_e32 v76, v0
	s_lshl_b64 s[6:7], s[6:7], 10
	v_pk_mul_f32 v[72:73], v[36:37], v[72:73] op_sel_hi:[0,1]
	v_cvt_pk_fp8_f32 v37, v74, v75 op_sel:[0,0,1]
	v_pk_fma_f32 v[72:73], v[72:73], v[24:25], v[6:7]
	v_lshl_add_u64 v[80:81], v[112:113], 0, s[6:7]
	v_cvt_pk_fp8_f32 v76, v72, v73
	v_pk_mul_f32 v[70:71], v[36:37], v[70:71] op_sel_hi:[0,1]
	v_pk_fma_f32 v[70:71], v[70:71], v[22:23], v[8:9]
	v_pk_mul_f32 v[68:69], v[36:37], v[68:69] op_sel_hi:[0,1]
	v_cvt_pk_fp8_f32 v76, v70, v71 op_sel:[0,0,1]
	v_pk_fma_f32 v[68:69], v[68:69], v[28:29], v[10:11]
	v_mov_b32_e32 v70, v0
	v_pk_mul_f32 v[40:41], v[36:37], v[40:41] op_sel_hi:[0,1]
	v_cvt_pk_fp8_f32 v70, v68, v69
	v_pk_fma_f32 v[40:41], v[40:41], v[32:33], v[14:15]
	v_mov_b32_e32 v68, v0
	v_cvt_pk_fp8_f32 v68, v40, v41
	v_pk_mul_f32 v[42:43], v[36:37], v[42:43] op_sel_hi:[0,1]
	v_pk_fma_f32 v[42:43], v[42:43], v[26:27], v[12:13]
	v_pk_mul_f32 v[38:39], v[36:37], v[38:39] op_sel_hi:[0,1]
	v_cvt_pk_fp8_f32 v70, v42, v43 op_sel:[0,0,1]
	v_pk_fma_f32 v[38:39], v[38:39], v[30:31], v[16:17]
	s_nop 0
	v_cvt_pk_fp8_f32 v68, v38, v39 op_sel:[0,0,1]
	global_store_dword v[80:81], v37, off
	global_store_dword v[80:81], v76, off offset:256
	global_store_dword v[80:81], v70, off offset:512
	global_store_dword v[80:81], v68, off offset:768
	s_and_saveexec_b64 s[6:7], s[4:5]
	s_cbranch_execz .LBB0_800
	s_and_b32 s14, s9, 0x3ffffff0
	v_lshl_add_u32 v37, s14, 2, v161
	ds_read_b32 v38, v37
	s_cmpk_lt_i32 s13, 0x80
	s_cbranch_scc1 .LBB0_799
	s_waitcnt lgkmcnt(0)
	ds_read2st64_b32 v[38:39], v79 offset0:4 offset1:8
	s_waitcnt lgkmcnt(0)
	v_add_f32_e32 v38, 0, v38
	v_add_f32_e32 v40, v38, v39
	ds_read2st64_b32 v[38:39], v79 offset0:12 offset1:16
	s_waitcnt lgkmcnt(0)
	v_add_f32_e32 v38, v40, v38
	v_add_f32_e32 v40, v38, v39
	ds_read2st64_b32 v[38:39], v79 offset0:20 offset1:24
	s_waitcnt lgkmcnt(0)
	v_add_f32_e32 v38, v40, v38
	v_add_f32_e32 v40, v38, v39
	ds_read2st64_b32 v[38:39], v79 offset0:28 offset1:32
	s_waitcnt lgkmcnt(0)
	v_add_f32_e32 v38, v40, v38
	v_add_f32_e32 v38, v38, v39

.LBB0_801:
	s_min_i32 s6, s10, s2
	s_ashr_i32 s7, s6, 31
	s_lshl_b64 s[6:7], s[6:7], 11
	s_waitcnt lgkmcnt(0)
	v_lshl_add_u64 v[36:37], v[34:35], 0, s[6:7]
	global_load_dwordx2 v[42:43], v[36:37], off
	global_load_dwordx2 v[40:41], v[36:37], off offset:512
	global_load_dwordx2 v[38:39], v[36:37], off offset:1024
	s_nop 0
	global_load_dwordx2 v[36:37], v[36:37], off offset:1536
	s_waitcnt vmcnt(15)
	v_and_b32_e32 v77, 0xffff0000, v66
	v_and_b32_e32 v75, 0xffff0000, v67
	v_lshlrev_b32_e32 v76, 16, v66
	v_lshlrev_b32_e32 v74, 16, v67
	s_waitcnt vmcnt(14)
	v_lshlrev_b32_e32 v72, 16, v64
	v_and_b32_e32 v73, 0xffff0000, v64
	v_lshlrev_b32_e32 v70, 16, v65
	v_and_b32_e32 v71, 0xffff0000, v65
	s_waitcnt vmcnt(13)
	v_lshlrev_b32_e32 v68, 16, v62
	v_and_b32_e32 v69, 0xffff0000, v62
	v_lshlrev_b32_e32 v66, 16, v63
	v_and_b32_e32 v67, 0xffff0000, v63
	s_waitcnt vmcnt(12)
	v_lshlrev_b32_e32 v64, 16, v60
	v_and_b32_e32 v65, 0xffff0000, v60
	v_lshlrev_b32_e32 v62, 16, v61
	v_and_b32_e32 v63, 0xffff0000, v61
	v_mul_f32_e32 v60, v77, v77
	v_mul_f32_e32 v61, v75, v75
	v_fmac_f32_e32 v60, v76, v76
	v_fmac_f32_e32 v61, v74, v74
	v_add_f32_e32 v60, v60, v61
	v_mul_f32_e32 v61, v73, v73
	v_mul_f32_e32 v80, v71, v71
	v_fmac_f32_e32 v61, v72, v72
	v_fmac_f32_e32 v80, v70, v70
	v_add_f32_e32 v61, v61, v80
	v_add_f32_e32 v60, v60, v61
	v_mul_f32_e32 v61, v69, v69
	v_mul_f32_e32 v80, v67, v67
	v_fmac_f32_e32 v61, v68, v68
	v_fmac_f32_e32 v80, v66, v66
	v_add_f32_e32 v61, v61, v80
	v_add_f32_e32 v60, v60, v61
	v_mul_f32_e32 v61, v65, v65
	v_mul_f32_e32 v80, v63, v63
	v_fmac_f32_e32 v61, v64, v64
	v_fmac_f32_e32 v80, v62, v62
	v_add_f32_e32 v61, v61, v80
	v_add_f32_e32 v60, v60, v61
	s_cmp_ge_i32 s11, s67
	s_waitcnt lgkmcnt(0)
	s_nop 1
	v_add_f32_dpp v60, v60, v60 quad_perm:[1,0,3,2] row_mask:0xf bank_mask:0xf
	s_waitcnt lgkmcnt(0)
	s_nop 1
	v_add_f32_dpp v60, v60, v60 quad_perm:[2,3,0,1] row_mask:0xf bank_mask:0xf
	s_waitcnt lgkmcnt(0)
	s_nop 1
	v_add_f32_dpp v60, v60, v60 row_half_mirror row_mask:0xf bank_mask:0xf
	s_waitcnt lgkmcnt(0)
	s_nop 1
	v_add_f32_dpp v60, v60, v60 row_mirror row_mask:0xf bank_mask:0xf
	s_waitcnt lgkmcnt(0)
	s_nop 1
	v_add_f32_dpp v60, v60, v60 row_bcast:15 row_mask:0xa bank_mask:0xf
	s_cbranch_scc1 .LBB0_782
	s_waitcnt lgkmcnt(0)
	s_nop 1
	v_add_f32_dpp v60, v60, v60 row_bcast:31 row_mask:0xc bank_mask:0xf
	s_nop 0
	v_readlane_b32 s101, v60, 63
	s_nop 1
	v_mov_b32_e32 v60, s101
	v_fmamk_f32 v60, v60, 0x3a800000, v210
	v_rsq_f32_e32 v60, v60
	s_add_i32 s6, s88, s10
	s_sub_i32 s6, s6, 24
	s_ashr_i32 s7, s6, 31
	v_pk_mul_f32 v[76:77], v[60:61], v[76:77] op_sel_hi:[0,1]
	v_pk_mul_f32 v[74:75], v[60:61], v[74:75] op_sel_hi:[0,1]
	v_pk_fma_f32 v[76:77], v[76:77], v[20:21], v[2:3]
	v_mov_b32_e32 v61, v0
	v_cvt_pk_fp8_f32 v61, v76, v77
	v_pk_fma_f32 v[74:75], v[74:75], v[18:19], v[4:5]
	v_mov_b32_e32 v76, v0
	s_lshl_b64 s[6:7], s[6:7], 10
	v_pk_mul_f32 v[72:73], v[60:61], v[72:73] op_sel_hi:[0,1]
	v_cvt_pk_fp8_f32 v61, v74, v75 op_sel:[0,0,1]
	v_pk_fma_f32 v[72:73], v[72:73], v[24:25], v[6:7]
	v_lshl_add_u64 v[80:81], v[112:113], 0, s[6:7]
	v_cvt_pk_fp8_f32 v76, v72, v73
	v_pk_mul_f32 v[70:71], v[60:61], v[70:71] op_sel_hi:[0,1]
	v_pk_fma_f32 v[70:71], v[70:71], v[22:23], v[8:9]
	v_pk_mul_f32 v[68:69], v[60:61], v[68:69] op_sel_hi:[0,1]
	v_cvt_pk_fp8_f32 v76, v70, v71 op_sel:[0,0,1]
	v_pk_fma_f32 v[68:69], v[68:69], v[28:29], v[10:11]
	v_mov_b32_e32 v70, v0
	v_pk_mul_f32 v[64:65], v[60:61], v[64:65] op_sel_hi:[0,1]
	v_cvt_pk_fp8_f32 v70, v68, v69
	v_pk_fma_f32 v[64:65], v[64:65], v[32:33], v[14:15]
	v_mov_b32_e32 v68, v0
	v_cvt_pk_fp8_f32 v68, v64, v65
	v_pk_mul_f32 v[66:67], v[60:61], v[66:67] op_sel_hi:[0,1]
	v_pk_fma_f32 v[66:67], v[66:67], v[26:27], v[12:13]
	v_pk_mul_f32 v[62:63], v[60:61], v[62:63] op_sel_hi:[0,1]
	v_cvt_pk_fp8_f32 v70, v66, v67 op_sel:[0,0,1]
	v_pk_fma_f32 v[62:63], v[62:63], v[30:31], v[16:17]
	s_nop 0
	v_cvt_pk_fp8_f32 v68, v62, v63 op_sel:[0,0,1]
	global_store_dword v[80:81], v61, off
	global_store_dword v[80:81], v76, off offset:256
	global_store_dword v[80:81], v70, off offset:512
	global_store_dword v[80:81], v68, off offset:768
	s_and_saveexec_b64 s[6:7], s[4:5]
	s_cbranch_execz .LBB0_781
	s_add_i32 s13, s9, 16
	s_and_b32 s13, s13, 0x3ffffff0
	v_lshl_add_u32 v61, s13, 2, v161
	ds_read_b32 v62, v61
	s_cmpk_lt_i32 s11, 0x80
	s_cbranch_scc1 .LBB0_780
	s_waitcnt lgkmcnt(0)
	ds_read2st64_b32 v[62:63], v79 offset0:6 offset1:10
	s_waitcnt lgkmcnt(0)
	v_add_f32_e32 v62, 0, v62
	v_add_f32_e32 v64, v62, v63
	ds_read2st64_b32 v[62:63], v79 offset0:14 offset1:18
	s_waitcnt lgkmcnt(0)
	v_add_f32_e32 v62, v64, v62
	v_add_f32_e32 v64, v62, v63
	ds_read2st64_b32 v[62:63], v79 offset0:22 offset1:26
	s_waitcnt lgkmcnt(0)
	v_add_f32_e32 v62, v64, v62
	v_add_f32_e32 v64, v62, v63
	ds_read2st64_b32 v[62:63], v79 offset0:30 offset1:34
	s_waitcnt lgkmcnt(0)
	v_add_f32_e32 v62, v64, v62
	v_add_f32_e32 v62, v62, v63
	s_branch .LBB0_780

.LBB0_1201:
	s_ashr_i32 s0, s25, 31
	s_lshr_b32 s0, s0, 20
	s_add_i32 s0, s25, s0
	s_ashr_i32 s40, s0, 12
	s_and_b32 s41, s0, 0xfffff000
	v_mad_i64_i32 v[50:51], s[0:1], s40, v62, v[18:19]
	s_mul_hi_i32 s0, s40, 0x1100
	s_mulk_i32 s40, 0x1100
	s_ashr_i32 s1, s41, 31
	s_sub_u32 s40, s40, s41
	s_subb_u32 s1, s0, s1
	s_add_u32 s0, s38, s40
	s_addc_u32 s1, s39, s1
	s_lshl_b64 s[0:1], s[0:1], 11
	global_load_dwordx4 v[34:37], v[50:51], off
	global_load_dwordx4 v[38:41], v[50:51], off offset:1024
	global_load_dwordx4 v[42:45], v[50:51], off offset:2048
	global_load_dwordx4 v[46:49], v[50:51], off offset:3072
	v_lshl_add_u64 v[50:51], v[20:21], 0, s[0:1]
	v_lshl_add_u64 v[52:53], v[22:23], 0, s[0:1]
	global_load_dwordx2 v[54:55], v[50:51], off
	global_load_dword v33, v[52:53], off
	global_load_dword v63, v[52:53], off offset:1024
	global_load_dwordx2 v[56:57], v[50:51], off offset:512
	global_load_dword v76, v[52:53], off offset:256
	global_load_dword v80, v[52:53], off offset:1280
	global_load_dwordx2 v[58:59], v[50:51], off offset:1024
	global_load_dword v86, v[52:53], off offset:512
	global_load_dword v90, v[52:53], off offset:1536
	global_load_dwordx2 v[64:65], v[50:51], off offset:1536
	global_load_dword v100, v[52:53], off offset:1792
	global_load_dword v96, v[52:53], off offset:768
	s_add_i32 s25, s25, s28
	s_add_u32 s38, s38, s28
	s_addc_u32 s39, s39, s29
	s_cmp_lt_i32 s25, 0x8000
	s_waitcnt vmcnt(11)
	v_lshlrev_b32_e32 v50, 16, v54
	v_and_b32_e32 v51, 0xffff0000, v54
	v_lshlrev_b32_e32 v52, 16, v55
	v_and_b32_e32 v53, 0xffff0000, v55
	s_waitcnt vmcnt(10)
	v_cvt_pk_f32_fp8_e32 v[54:55], v33
	v_cvt_pk_f32_fp8_sdwa v[66:67], v33 src0_sel:WORD_1
	s_waitcnt vmcnt(9)
	v_cvt_pk_f32_fp8_e32 v[68:69], v63
	v_cvt_pk_f32_fp8_sdwa v[70:71], v63 src0_sel:WORD_1
	s_waitcnt vmcnt(7)
	v_cvt_pk_f32_fp8_e32 v[74:75], v76
	v_cvt_pk_f32_fp8_sdwa v[76:77], v76 src0_sel:WORD_1
	s_waitcnt vmcnt(6)
	v_cvt_pk_f32_fp8_e32 v[78:79], v80
	v_cvt_pk_f32_fp8_sdwa v[80:81], v80 src0_sel:WORD_1
	s_waitcnt vmcnt(4)
	v_cvt_pk_f32_fp8_e32 v[84:85], v86
	v_cvt_pk_f32_fp8_sdwa v[86:87], v86 src0_sel:WORD_1
	s_waitcnt vmcnt(3)
	v_cvt_pk_f32_fp8_e32 v[88:89], v90
	v_cvt_pk_f32_fp8_sdwa v[90:91], v90 src0_sel:WORD_1
	s_waitcnt vmcnt(0)
	v_cvt_pk_f32_fp8_e32 v[94:95], v96
	v_cvt_pk_f32_fp8_sdwa v[96:97], v96 src0_sel:WORD_1
	v_cvt_pk_f32_fp8_e32 v[98:99], v100
	v_cvt_pk_f32_fp8_sdwa v[100:101], v100 src0_sel:WORD_1
	v_pk_mul_f32 v[36:37], v[36:37], s[6:7] op_sel_hi:[1,0]
	v_pk_mul_f32 v[34:35], v[34:35], s[6:7] op_sel_hi:[1,0]
	v_pk_mul_f32 v[40:41], v[40:41], s[6:7] op_sel_hi:[1,0]
	v_pk_mul_f32 v[38:39], v[38:39], s[6:7] op_sel_hi:[1,0]
	v_lshlrev_b32_e32 v72, 16, v56
	v_and_b32_e32 v73, 0xffff0000, v56
	v_lshlrev_b32_e32 v56, 16, v57
	v_and_b32_e32 v57, 0xffff0000, v57
	v_pk_add_f32 v[54:55], v[54:55], v[68:69]
	v_pk_add_f32 v[66:67], v[66:67], v[70:71]
	v_pk_add_f32 v[68:69], v[74:75], v[78:79]
	v_pk_add_f32 v[70:71], v[76:77], v[80:81]
	v_pk_fma_f32 v[34:35], v[34:35], v[54:55], v[50:51]
	v_pk_fma_f32 v[36:37], v[36:37], v[66:67], v[52:53]
	v_pk_fma_f32 v[38:39], v[38:39], v[68:69], v[72:73]
	v_pk_fma_f32 v[40:41], v[40:41], v[70:71], v[56:57]
	v_pk_mul_f32 v[42:43], v[42:43], s[6:7] op_sel_hi:[1,0]
	v_pk_mul_f32 v[44:45], v[44:45], s[6:7] op_sel_hi:[1,0]
	v_pk_mul_f32 v[48:49], v[48:49], s[6:7] op_sel_hi:[1,0]
	v_lshlrev_b32_e32 v82, 16, v58
	v_and_b32_e32 v83, 0xffff0000, v58
	v_lshlrev_b32_e32 v58, 16, v59
	v_and_b32_e32 v59, 0xffff0000, v59
	v_lshlrev_b32_e32 v92, 16, v64
	v_and_b32_e32 v93, 0xffff0000, v64
	v_lshlrev_b32_e32 v64, 16, v65
	v_and_b32_e32 v65, 0xffff0000, v65
	v_pk_add_f32 v[74:75], v[84:85], v[88:89]
	v_pk_add_f32 v[76:77], v[86:87], v[90:91]
	v_pk_add_f32 v[80:81], v[96:97], v[100:101]
	v_pk_mul_f32 v[50:51], v[36:37], v[36:37]
	v_pk_mul_f32 v[52:53], v[34:35], v[34:35]
	v_pk_mul_f32 v[54:55], v[40:41], v[40:41]
	v_pk_mul_f32 v[56:57], v[38:39], v[38:39]
	v_pk_mul_f32 v[46:47], v[46:47], s[6:7] op_sel_hi:[1,0]
	v_pk_add_f32 v[78:79], v[94:95], v[98:99]
	v_pk_fma_f32 v[44:45], v[44:45], v[76:77], v[58:59]
	v_pk_fma_f32 v[42:43], v[42:43], v[74:75], v[82:83]
	v_pk_fma_f32 v[48:49], v[48:49], v[80:81], v[64:65]
	v_pk_mov_b32 v[66:67], v[52:53], v[50:51] op_sel:[1,0]
	v_mov_b32_e32 v53, v51
	v_pk_mov_b32 v[50:51], v[56:57], v[54:55] op_sel:[1,0]
	v_mov_b32_e32 v57, v55
	v_pk_fma_f32 v[46:47], v[46:47], v[78:79], v[92:93]
	v_mul_f32_e32 v65, v48, v48
	v_mul_f32_e32 v58, v43, v43
	v_mul_f32_e32 v64, v45, v45
	v_pk_add_f32 v[52:53], v[66:67], v[52:53]
	v_pk_add_f32 v[50:51], v[50:51], v[56:57]
	v_mul_f32_e32 v33, v46, v46
	v_mul_f32_e32 v63, v47, v47
	v_mul_f32_e32 v68, v49, v49
	v_pk_fma_f32 v[54:55], v[42:43], v[42:43], v[58:59] op_sel_hi:[1,1,0]
	v_pk_fma_f32 v[58:59], v[44:45], v[44:45], v[64:65] op_sel_hi:[1,1,0]
	v_pk_add_f32 v[52:53], v[52:53], v[52:53] op_sel:[0,1] op_sel_hi:[1,0]
	v_pk_add_f32 v[50:51], v[50:51], v[50:51] op_sel:[0,1] op_sel_hi:[1,0]
	v_mov_b32_e32 v55, v65
	v_mov_b32_e32 v59, v68
	v_mov_b32_e32 v53, v33
	v_mov_b32_e32 v51, v63
	v_pk_add_f32 v[54:55], v[54:55], v[58:59]
	v_pk_add_f32 v[50:51], v[52:53], v[50:51]
	s_nop 0
	v_pk_add_f32 v[50:51], v[50:51], v[54:55]
	s_nop 0
	v_add_f32_e32 v33, v50, v51
	s_waitcnt lgkmcnt(0)
	s_nop 1
	v_add_f32_dpp v33, v33, v33 quad_perm:[1,0,3,2] row_mask:0xf bank_mask:0xf
	s_waitcnt lgkmcnt(0)
	s_nop 1
	v_add_f32_dpp v33, v33, v33 quad_perm:[2,3,0,1] row_mask:0xf bank_mask:0xf
	s_waitcnt lgkmcnt(0)
	s_nop 1
	v_add_f32_dpp v33, v33, v33 row_half_mirror row_mask:0xf bank_mask:0xf
	s_waitcnt lgkmcnt(0)
	s_nop 1
	v_add_f32_dpp v33, v33, v33 row_mirror row_mask:0xf bank_mask:0xf
	s_waitcnt lgkmcnt(0)
	s_nop 1
	v_add_f32_dpp v33, v33, v33 row_bcast:15 row_mask:0xa bank_mask:0xf
	s_waitcnt lgkmcnt(0)
	s_nop 1
	v_add_f32_dpp v33, v33, v33 row_bcast:31 row_mask:0xc bank_mask:0xf
	s_nop 0
	v_readlane_b32 s101, v33, 63
	s_nop 1
	v_mov_b32_e32 v33, s101
	v_fmamk_f32 v33, v33, 0x3a800000, v60
	v_mul_f32_e32 v50, 0x4f800000, v33
	v_cmp_gt_f32_e32 vcc, s33, v33
	s_nop 1
	v_cndmask_b32_e32 v33, v33, v50, vcc
	v_sqrt_f32_e32 v50, v33
	s_nop 0
	v_add_u32_e32 v51, -1, v50
	v_add_u32_e32 v52, 1, v50
	v_fma_f32 v53, -v51, v50, v33
	v_fma_f32 v54, -v52, v50, v33
	v_cmp_ge_f32_e64 s[0:1], 0, v53
	s_nop 1
	v_cndmask_b32_e64 v50, v50, v51, s[0:1]
	v_cmp_lt_f32_e64 s[0:1], 0, v54
	s_nop 1
	v_cndmask_b32_e64 v50, v50, v52, s[0:1]
	v_mul_f32_e32 v51, 0x37800000, v50
	v_cndmask_b32_e32 v50, v50, v51, vcc
	v_cmp_class_f32_e32 vcc, v33, v61
	s_nop 1
	v_cndmask_b32_e32 v33, v50, v33, vcc
	v_div_scale_f32 v50, s[0:1], v33, v33, 1.0
	v_rcp_f32_e32 v52, v50
	v_div_scale_f32 v51, vcc, 1.0, v33, 1.0
	v_fma_f32 v53, -v50, v52, 1.0
	v_fmac_f32_e32 v52, v53, v52
	v_mul_f32_e32 v53, v51, v52
	v_fma_f32 v54, -v50, v53, v51
	v_fmac_f32_e32 v53, v54, v52
	v_fma_f32 v50, -v50, v53, v51
	v_div_fmas_f32 v50, v50, v52, v53
	v_div_fixup_f32 v50, v50, v33, 1.0
	v_pk_mul_f32 v[34:35], v[50:51], v[34:35] op_sel_hi:[0,1]
	v_pk_mul_f32 v[36:37], v[50:51], v[36:37] op_sel_hi:[0,1]
	v_pk_mul_f32 v[38:39], v[50:51], v[38:39] op_sel_hi:[0,1]
	v_pk_mul_f32 v[40:41], v[50:51], v[40:41] op_sel_hi:[0,1]
	v_pk_mul_f32 v[42:43], v[50:51], v[42:43] op_sel_hi:[0,1]
	v_pk_mul_f32 v[44:45], v[50:51], v[44:45] op_sel_hi:[0,1]
	v_pk_mul_f32 v[46:47], v[50:51], v[46:47] op_sel_hi:[0,1]
	v_pk_mul_f32 v[48:49], v[50:51], v[48:49] op_sel_hi:[0,1]
	v_pk_mul_f32 v[36:37], v[36:37], v[2:3]
	v_pk_mul_f32 v[34:35], v[34:35], v[0:1]
	v_pk_mul_f32 v[40:41], v[40:41], v[6:7]
	v_pk_mul_f32 v[38:39], v[38:39], v[4:5]
	v_pk_mul_f32 v[44:45], v[44:45], v[10:11]
	v_pk_mul_f32 v[42:43], v[42:43], v[8:9]
	v_pk_mul_f32 v[48:49], v[48:49], v[14:15]
	v_pk_mul_f32 v[46:47], v[46:47], v[12:13]
	global_store_dwordx4 v[24:25], v[34:37], off offset:-2048
	global_store_dwordx4 v[24:25], v[38:41], off offset:-1024
	global_store_dwordx4 v[24:25], v[42:45], off
	global_store_dwordx4 v[24:25], v[46:49], off offset:1024
	v_lshl_add_u64 v[24:25], v[24:25], 0, s[30:31]
	s_cbranch_scc1 .LBB0_1201

.LBB0_1205:
	s_waitcnt vmcnt(11)
	v_cvt_pk_f32_fp8_e32 v[86:87], v83
	v_cvt_pk_f32_fp8_sdwa v[88:89], v83 src0_sel:WORD_1
	s_waitcnt vmcnt(10)
	v_cvt_pk_f32_fp8_e32 v[90:91], v82
	v_cvt_pk_f32_fp8_sdwa v[82:83], v82 src0_sel:WORD_1
	v_lshlrev_b32_e32 v84, 16, v58
	v_and_b32_e32 v85, 0xffff0000, v58
	v_lshlrev_b32_e32 v58, 16, v59
	v_and_b32_e32 v59, 0xffff0000, v59
	v_pk_add_f32 v[86:87], v[86:87], v[90:91]
	v_pk_add_f32 v[82:83], v[88:89], v[82:83]
	v_pk_fma_f32 v[84:85], v[34:35], v[86:87], v[84:85]
	v_pk_fma_f32 v[58:59], v[32:33], v[82:83], v[58:59]
	v_pk_mul_f32 v[86:87], v[84:85], v[84:85]
	v_pk_mul_f32 v[82:83], v[58:59], v[58:59]
	s_waitcnt vmcnt(9)
	v_cvt_pk_f32_fp8_sdwa v[90:91], v81 src0_sel:WORD_1
	v_pk_mov_b32 v[88:89], v[86:87], v[82:83] op_sel:[1,0]
	v_mov_b32_e32 v87, v83
	v_pk_add_f32 v[82:83], v[88:89], v[86:87]
	v_cvt_pk_f32_fp8_e32 v[88:89], v81
	s_waitcnt vmcnt(8)
	v_cvt_pk_f32_fp8_e32 v[92:93], v80
	v_cvt_pk_f32_fp8_sdwa v[80:81], v80 src0_sel:WORD_1
	v_lshlrev_b32_e32 v86, 16, v56
	v_and_b32_e32 v87, 0xffff0000, v56
	v_lshlrev_b32_e32 v56, 16, v57
	v_and_b32_e32 v57, 0xffff0000, v57
	v_pk_add_f32 v[88:89], v[88:89], v[92:93]
	v_pk_add_f32 v[80:81], v[90:91], v[80:81]
	v_pk_fma_f32 v[86:87], v[38:39], v[88:89], v[86:87]
	v_pk_fma_f32 v[56:57], v[36:37], v[80:81], v[56:57]
	v_pk_mul_f32 v[88:89], v[86:87], v[86:87]
	v_pk_mul_f32 v[80:81], v[56:57], v[56:57]
	s_waitcnt vmcnt(6)
	v_cvt_pk_f32_fp8_e32 v[94:95], v78
	v_pk_mov_b32 v[90:91], v[88:89], v[80:81] op_sel:[1,0]
	v_mov_b32_e32 v89, v81
	v_pk_add_f32 v[80:81], v[90:91], v[88:89]
	v_cvt_pk_f32_fp8_e32 v[90:91], v79
	v_cvt_pk_f32_fp8_sdwa v[92:93], v79 src0_sel:WORD_1
	v_cvt_pk_f32_fp8_sdwa v[78:79], v78 src0_sel:WORD_1
	v_lshlrev_b32_e32 v88, 16, v54
	v_and_b32_e32 v89, 0xffff0000, v54
	v_pk_add_f32 v[90:91], v[90:91], v[94:95]
	s_waitcnt vmcnt(5)
	v_cvt_pk_f32_fp8_e32 v[94:95], v16
	v_pk_fma_f32 v[88:89], v[42:43], v[90:91], v[88:89]
	s_waitcnt vmcnt(4)
	v_cvt_pk_f32_fp8_e32 v[90:91], v77
	v_pk_add_f32 v[78:79], v[92:93], v[78:79]
	v_cvt_pk_f32_fp8_sdwa v[92:93], v77 src0_sel:WORD_1
	v_cvt_pk_f32_fp8_sdwa v[96:97], v16 src0_sel:WORD_1
	v_lshlrev_b32_e32 v54, 16, v55
	v_and_b32_e32 v55, 0xffff0000, v55
	v_pk_fma_f32 v[78:79], v[40:41], v[78:79], v[54:55]
	v_lshlrev_b32_e32 v54, 16, v52
	v_and_b32_e32 v55, 0xffff0000, v52
	v_pk_add_f32 v[90:91], v[90:91], v[94:95]
	v_lshlrev_b32_e32 v52, 16, v53
	v_and_b32_e32 v53, 0xffff0000, v53
	v_pk_add_f32 v[92:93], v[92:93], v[96:97]
	v_pk_fma_f32 v[90:91], v[46:47], v[90:91], v[54:55]
	v_pk_fma_f32 v[92:93], v[44:45], v[92:93], v[52:53]
	v_mul_f32_e32 v16, v90, v90
	v_mul_f32_e32 v77, v91, v91
	v_pk_add_f32 v[52:53], v[82:83], v[82:83] op_sel:[0,1] op_sel_hi:[1,0]
	v_pk_add_f32 v[54:55], v[80:81], v[80:81] op_sel:[0,1] op_sel_hi:[1,0]
	v_mov_b32_e32 v53, v16
	v_mov_b32_e32 v55, v77
	v_mul_f32_e32 v16, v89, v89
	v_pk_add_f32 v[52:53], v[52:53], v[54:55]
	v_pk_fma_f32 v[54:55], v[88:89], v[88:89], v[16:17] op_sel_hi:[1,1,0]
	v_mul_f32_e32 v16, v79, v79
	v_mul_f32_e32 v94, v92, v92
	v_mul_f32_e32 v95, v93, v93
	v_pk_fma_f32 v[80:81], v[78:79], v[78:79], v[16:17] op_sel_hi:[1,1,0]
	v_mov_b32_e32 v55, v94
	v_mov_b32_e32 v81, v95
	v_pk_add_f32 v[54:55], v[54:55], v[80:81]
	s_add_i32 s21, s21, 2
	v_pk_add_f32 v[52:53], v[52:53], v[54:55]
	v_lshl_add_u64 v[30:31], v[30:31], 0, s[14:15]
	v_add_f32_e32 v16, v52, v53
	v_lshl_add_u64 v[50:51], v[50:51], 0, s[14:15]
	s_waitcnt lgkmcnt(0)
	s_nop 1
	v_add_f32_dpp v16, v16, v16 quad_perm:[1,0,3,2] row_mask:0xf bank_mask:0xf
	s_waitcnt lgkmcnt(0)
	s_nop 1
	v_add_f32_dpp v16, v16, v16 quad_perm:[2,3,0,1] row_mask:0xf bank_mask:0xf
	s_waitcnt lgkmcnt(0)
	s_nop 1
	v_add_f32_dpp v16, v16, v16 row_half_mirror row_mask:0xf bank_mask:0xf
	s_waitcnt lgkmcnt(0)
	s_nop 1
	v_add_f32_dpp v16, v16, v16 row_mirror row_mask:0xf bank_mask:0xf
	s_waitcnt lgkmcnt(0)
	s_nop 1
	v_add_f32_dpp v16, v16, v16 row_bcast:15 row_mask:0xa bank_mask:0xf
	s_waitcnt lgkmcnt(0)
	s_nop 1
	v_add_f32_dpp v16, v16, v16 row_bcast:31 row_mask:0xc bank_mask:0xf
	s_nop 0
	v_readlane_b32 s101, v16, 63
	s_nop 1
	v_mov_b32_e32 v16, s101
	v_fmamk_f32 v16, v16, 0x3a800000, v60
	v_mul_f32_e32 v52, 0x4f800000, v16
	v_cmp_gt_f32_e32 vcc, s33, v16
	s_nop 1
	v_cndmask_b32_e32 v16, v16, v52, vcc
	v_sqrt_f32_e32 v52, v16
	s_nop 0
	v_add_u32_e32 v53, -1, v52
	v_fma_f32 v54, -v53, v52, v16
	v_cmp_ge_f32_e64 s[0:1], 0, v54
	v_add_u32_e32 v54, 1, v52
	s_nop 0
	v_cndmask_b32_e64 v53, v52, v53, s[0:1]
	v_fma_f32 v52, -v54, v52, v16
	v_cmp_lt_f32_e64 s[0:1], 0, v52
	s_nop 1
	v_cndmask_b32_e64 v52, v53, v54, s[0:1]
	v_mul_f32_e32 v53, 0x37800000, v52
	v_cndmask_b32_e32 v52, v52, v53, vcc
	v_cmp_class_f32_e32 vcc, v16, v61
	s_nop 1
	v_cndmask_b32_e32 v16, v52, v16, vcc
	v_div_scale_f32 v52, s[0:1], v16, v16, 1.0
	v_rcp_f32_e32 v53, v52
	s_nop 0
	v_fma_f32 v54, -v52, v53, 1.0
	v_fmac_f32_e32 v53, v54, v53
	v_div_scale_f32 v54, vcc, 1.0, v16, 1.0
	v_mul_f32_e32 v55, v54, v53
	v_fma_f32 v77, -v52, v55, v54
	v_fmac_f32_e32 v55, v77, v53
	v_fma_f32 v52, -v52, v55, v54
	v_div_fmas_f32 v52, v52, v53, v55
	v_div_fixup_f32 v16, v52, v16, 1.0
	v_pk_mul_f32 v[52:53], v[16:17], v[84:85] op_sel_hi:[0,1]
	v_pk_mul_f32 v[54:55], v[16:17], v[58:59] op_sel_hi:[0,1]
	v_pk_mul_f32 v[54:55], v[54:55], v[2:3]
	v_pk_mul_f32 v[52:53], v[52:53], v[0:1]
	global_store_dwordx4 v[48:49], v[52:55], off offset:-3072
	s_and_b64 vcc, exec, s[18:19]
	s_nop 0
	v_pk_mul_f32 v[52:53], v[16:17], v[86:87] op_sel_hi:[0,1]
	v_pk_mul_f32 v[54:55], v[16:17], v[56:57] op_sel_hi:[0,1]
	v_pk_mul_f32 v[54:55], v[54:55], v[6:7]
	v_pk_mul_f32 v[52:53], v[52:53], v[4:5]
	global_store_dwordx4 v[48:49], v[52:55], off offset:-2048
	s_nop 1
	v_pk_mul_f32 v[52:53], v[16:17], v[88:89] op_sel_hi:[0,1]
	v_pk_mul_f32 v[54:55], v[16:17], v[78:79] op_sel_hi:[0,1]
	v_pk_mul_f32 v[54:55], v[54:55], v[10:11]
	v_pk_mul_f32 v[52:53], v[52:53], v[8:9]
	global_store_dwordx4 v[48:49], v[52:55], off offset:-1024
	s_nop 1
	v_pk_mul_f32 v[52:53], v[16:17], v[90:91] op_sel_hi:[0,1]
	v_pk_mul_f32 v[54:55], v[16:17], v[92:93] op_sel_hi:[0,1]
	v_pk_mul_f32 v[54:55], v[54:55], v[14:15]
	v_pk_mul_f32 v[52:53], v[52:53], v[12:13]
	global_store_dwordx4 v[48:49], v[52:55], off
	v_lshl_add_u64 v[48:49], v[48:49], 0, s[16:17]
	s_cbranch_vccnz .LBB0_1197
